# MoE GEMM1 epilogue rewritten with packed f32 ops (v_pk_mul/fma/add_f32), same per-element operations; plus DPP lane exchanges in attention epilogue
# speedup vs baseline: 1.0990x; 1.0100x over previous
.LBB0_559:
	s_nop 5
	v_rcp_f32_e32 v144, v0
	v_rcp_f32_e32 v145, v1
	v_rcp_f32_e32 v142, v2
	v_rcp_f32_e32 v143, v3
	v_rcp_f32_e32 v140, v4
	v_rcp_f32_e32 v141, v5
	v_rcp_f32_e32 v138, v6
	v_rcp_f32_e32 v139, v7
	v_ashrrev_i32_e32 v209, 31, v208
	v_lshl_add_u64 v[136:137], v[208:209], 4, s[28:29]
	s_mov_b64 s[0:1], -1
	s_and_b64 vcc, exec, s[38:39]
	s_cbranch_vccz .LBB0_561
	v_add_co_u32_e32 v0, vcc, 0x2000, v136
	global_load_dwordx4 v[120:123], v[136:137], off
	s_nop 0
	v_addc_co_u32_e32 v1, vcc, 0, v137, vcc
	global_load_dwordx4 v[104:107], v[0:1], off
	v_add_co_u32_e32 v0, vcc, 0x4000, v136
	s_mov_b32 s0, 0x10000
	s_nop 0
	v_addc_co_u32_e32 v1, vcc, 0, v137, vcc
	global_load_dwordx4 v[88:91], v[0:1], off
	v_add_co_u32_e32 v0, vcc, 0x6000, v136
	v_lshlrev_b32_e32 v146, 2, v217
	s_nop 0
	v_addc_co_u32_e32 v1, vcc, 0, v137, vcc
	v_add_co_u32_e32 v4, vcc, 0x8000, v136
	global_load_dwordx4 v[0:3], v[0:1], off
	s_nop 0
	v_addc_co_u32_e32 v5, vcc, 0, v137, vcc
	global_load_dwordx4 v[124:127], v[4:5], off
	v_add_co_u32_e32 v4, vcc, 0xa000, v136
	v_mul_f32_e32 v150, v213, v144
	s_nop 0
	v_addc_co_u32_e32 v5, vcc, 0, v137, vcc
	global_load_dwordx4 v[108:111], v[4:5], off
	v_add_co_u32_e32 v4, vcc, 0xc000, v136
	v_mov_b32_e32 v152, v64
	s_nop 0
	v_addc_co_u32_e32 v5, vcc, 0, v137, vcc
	global_load_dwordx4 v[92:95], v[4:5], off
	v_add_co_u32_e32 v4, vcc, 0xe000, v136
	v_mov_b32_e32 v153, v48
	s_nop 0
	v_addc_co_u32_e32 v5, vcc, 0, v137, vcc
	v_add_co_u32_e32 v80, vcc, s0, v136
	s_mov_b32 s0, 0x12000
	s_nop 0
	v_addc_co_u32_e32 v81, vcc, 0, v137, vcc
	global_load_dwordx4 v[4:7], v[4:5], off
	v_mov_b32_e32 v156, v32
	global_load_dwordx4 v[128:131], v[80:81], off
	v_add_co_u32_e32 v80, vcc, s0, v136
	s_mov_b32 s0, 0x14000
	s_nop 0
	v_addc_co_u32_e32 v81, vcc, 0, v137, vcc
	global_load_dwordx4 v[112:115], v[80:81], off
	v_add_co_u32_e32 v80, vcc, s0, v136
	s_mov_b32 s0, 0x16000
	s_nop 0
	v_addc_co_u32_e32 v81, vcc, 0, v137, vcc
	global_load_dwordx4 v[96:99], v[80:81], off
	v_add_co_u32_e32 v80, vcc, s0, v136
	s_mov_b32 s0, 0x18000
	s_nop 0
	v_addc_co_u32_e32 v81, vcc, 0, v137, vcc
	v_add_co_u32_e32 v84, vcc, s0, v136
	global_load_dwordx4 v[80:83], v[80:81], off
	s_nop 0
	v_addc_co_u32_e32 v85, vcc, 0, v137, vcc
	global_load_dwordx4 v[132:135], v[84:85], off
	s_mov_b32 s0, 0x1a000
	v_add_co_u32_e32 v84, vcc, s0, v136
	s_mov_b32 s0, 0x1c000
	s_nop 0
	v_addc_co_u32_e32 v85, vcc, 0, v137, vcc
	global_load_dwordx4 v[116:119], v[84:85], off
	v_add_co_u32_e32 v84, vcc, s0, v136
	s_mov_b32 s0, 0x1e000
	s_nop 0
	v_addc_co_u32_e32 v85, vcc, 0, v137, vcc
	global_load_dwordx4 v[100:103], v[84:85], off
	v_add_co_u32_e32 v84, vcc, s0, v136
	s_waitcnt vmcnt(14)
	v_mov_b32_e32 v154, v120
	v_addc_co_u32_e32 v85, vcc, 0, v137, vcc
	global_load_dwordx4 v[84:87], v[84:85], off
	s_nop 0
	global_load_dword v149, v146, s[18:19]
	global_load_dword v148, v146, s[18:19] offset:128
	global_load_dword v147, v146, s[18:19] offset:256
	s_nop 0
	global_load_dword v146, v146, s[18:19] offset:384
	v_mov_b32_e32 v157, v16
	s_mov_b32 s0, 0x3727c5ac
	s_mov_b32 s1, 0x800000
	v_lshlrev_b32_e32 v160, 9, v200
	s_waitcnt vmcnt(15)
	v_mov_b32_e32 v155, v124
	v_pk_fma_f32 v[152:153], v[152:153], v[150:151], v[154:155] op_sel_hi:[1,0,1] neg_lo:[1,0,0] neg_hi:[1,0,0]
	s_waitcnt vmcnt(11)
	v_mov_b32_e32 v158, v128
	v_pk_mul_f32 v[154:155], v[152:153], v[152:153]
	s_waitcnt vmcnt(7)
	v_mov_b32_e32 v159, v132
	v_pk_fma_f32 v[150:151], v[156:157], v[150:151], v[158:159] op_sel_hi:[1,0,1] neg_lo:[1,0,0] neg_hi:[1,0,0]
	v_add_f32_e32 v120, v154, v155
	v_pk_mul_f32 v[156:157], v[150:151], v[150:151]
	s_nop 0
	v_add_f32_e32 v120, v120, v156
	v_add_f32_e32 v120, v120, v157
	s_nop 1
	v_mov_b32_dpp v124, v120 quad_perm:[1,0,3,2] row_mask:0xf bank_mask:0xf
	s_waitcnt lgkmcnt(0)
	v_add_f32_e32 v120, v120, v124
	s_nop 1
	v_mov_b32_dpp v124, v120 quad_perm:[2,3,0,1] row_mask:0xf bank_mask:0xf
	s_waitcnt lgkmcnt(0)
	v_add_f32_e32 v120, v120, v124
	s_nop 1
	v_mov_b32_dpp v124, v120 row_half_mirror row_mask:0xf bank_mask:0xf
	s_nop 1
	v_mov_b32_dpp v124, v124 quad_perm:[3,2,1,0] row_mask:0xf bank_mask:0xf
	s_waitcnt lgkmcnt(0)
	v_add_f32_e32 v120, v120, v124
	s_nop 1
	v_mov_b32_dpp v124, v120 row_ror:8 row_mask:0xf bank_mask:0xf
	s_waitcnt lgkmcnt(0)
	v_add_f32_e32 v120, v120, v124
	ds_swizzle_b32 v124, v120 offset:swizzle(SWAP,16)
	s_waitcnt lgkmcnt(0)
	v_add_f32_e32 v120, v120, v124
	v_mov_b32_e32 v124, s0
	v_fmac_f32_e32 v124, 0x3c000000, v120
	v_cmp_gt_f32_e32 vcc, s1, v124
	v_mul_f32_e32 v120, 0x4b800000, v124
	s_mov_b32 s0, 0x3727c5ac
	v_cndmask_b32_e32 v120, v124, v120, vcc
	v_rsq_f32_e32 v120, v120
	s_nop 0
	v_mul_f32_e32 v124, 0x45800000, v120
	v_cndmask_b32_e32 v120, v120, v124, vcc
	v_mul_f32_e32 v120, v214, v120
	v_mul_f32_e32 v124, v152, v120
	v_mul_f32_e32 v128, v153, v120
	s_waitcnt vmcnt(3)
	v_mul_f32_e32 v124, v149, v124
	s_waitcnt vmcnt(2)
	v_mul_f32_e32 v128, v148, v128
	v_mul_f32_e32 v132, v150, v120
	v_mov_b32_e32 v150, v201
	v_cvt_pk_fp8_f32 v150, v124, v128
	v_mul_f32_e32 v120, v151, v120
	s_waitcnt vmcnt(1)
	v_mul_f32_e32 v132, v147, v132
	s_waitcnt vmcnt(0)
	v_mul_f32_e32 v120, v146, v120
	v_cvt_pk_fp8_f32 v150, v132, v120 op_sel:[0,0,1]
	v_add3_u32 v120, s89, v217, v160
	v_mul_f32_e32 v128, v213, v145
	v_mov_b32_e32 v151, v49
	v_lshrrev_b32_e32 v124, 8, v150
	ds_write_b8 v120, v150 offset:51200
	ds_write_b8 v120, v124 offset:51232
	ds_write_b8_d16_hi v120, v150 offset:51264
	v_lshrrev_b32_e32 v124, 24, v150
	ds_write_b8 v120, v124 offset:51296
	v_mov_b32_e32 v150, v65
	v_mov_b32_e32 v124, v121
	v_pk_fma_f32 v[124:125], v[150:151], v[128:129], v[124:125] op_sel_hi:[1,0,1] neg_lo:[1,0,0] neg_hi:[1,0,0]
	v_mov_b32_e32 v152, v33
	v_mov_b32_e32 v153, v17
	v_mov_b32_e32 v132, v129
	v_pk_mul_f32 v[150:151], v[124:125], v[124:125]
	v_pk_fma_f32 v[128:129], v[152:153], v[128:129], v[132:133] op_sel_hi:[1,0,1] neg_lo:[1,0,0] neg_hi:[1,0,0]
	v_add_f32_e32 v121, v150, v151
	v_pk_mul_f32 v[132:133], v[128:129], v[128:129]
	v_mov_b32_e32 v150, v34
	v_add_f32_e32 v121, v121, v132
	v_add_f32_e32 v121, v121, v133
	s_nop 1
	v_mov_b32_dpp v132, v121 quad_perm:[1,0,3,2] row_mask:0xf bank_mask:0xf
	v_mov_b32_e32 v133, v126
	v_mov_b32_e32 v151, v18
	v_mov_b32_e32 v152, v130
	v_mov_b32_e32 v153, v134
	s_waitcnt lgkmcnt(0)
	v_add_f32_e32 v121, v121, v132
	s_nop 1
	v_mov_b32_dpp v132, v121 quad_perm:[2,3,0,1] row_mask:0xf bank_mask:0xf
	v_mov_b32_e32 v134, v131
	s_waitcnt lgkmcnt(0)
	v_add_f32_e32 v121, v121, v132
	s_nop 1
	v_mov_b32_dpp v132, v121 row_half_mirror row_mask:0xf bank_mask:0xf
	s_nop 1
	v_mov_b32_dpp v132, v132 quad_perm:[3,2,1,0] row_mask:0xf bank_mask:0xf
	s_waitcnt lgkmcnt(0)
	v_add_f32_e32 v121, v121, v132
	s_nop 1
	v_mov_b32_dpp v132, v121 row_ror:8 row_mask:0xf bank_mask:0xf
	s_waitcnt lgkmcnt(0)
	v_add_f32_e32 v121, v121, v132
	ds_swizzle_b32 v132, v121 offset:swizzle(SWAP,16)
	s_waitcnt lgkmcnt(0)
	v_add_f32_e32 v121, v121, v132
	v_mov_b32_e32 v132, s0
	v_fmac_f32_e32 v132, 0x3c000000, v121
	v_cmp_gt_f32_e32 vcc, s1, v132
	v_mul_f32_e32 v121, 0x4b800000, v132
	s_mov_b32 s0, 0x3727c5ac
	v_cndmask_b32_e32 v121, v132, v121, vcc
	v_rsq_f32_e32 v121, v121
	s_nop 0
	v_mul_f32_e32 v132, 0x45800000, v121
	v_cndmask_b32_e32 v121, v121, v132, vcc
	v_mul_f32_e32 v121, v214, v121
	v_mul_f32_e32 v124, v124, v121
	v_mul_f32_e32 v125, v125, v121
	v_mul_f32_e32 v124, v149, v124
	v_mul_f32_e32 v125, v148, v125
	v_mul_f32_e32 v128, v128, v121
	v_mul_f32_e32 v121, v129, v121
	v_mov_b32_e32 v129, v201
	v_cvt_pk_fp8_f32 v129, v124, v125
	v_mul_f32_e32 v128, v147, v128
	v_mul_f32_e32 v121, v146, v121
	v_mul_f32_e32 v124, v213, v142
	v_cvt_pk_fp8_f32 v129, v128, v121 op_sel:[0,0,1]
	v_mov_b32_e32 v128, v66
	v_mov_b32_e32 v132, v122
	v_lshrrev_b32_e32 v121, 8, v129
	ds_write_b8 v120, v129 offset:51328
	ds_write_b8 v120, v121 offset:51360
	ds_write_b8_d16_hi v120, v129 offset:51392
	v_lshrrev_b32_e32 v121, 24, v129
	v_mov_b32_e32 v129, v50
	v_pk_fma_f32 v[128:129], v[128:129], v[124:125], v[132:133] op_sel_hi:[1,0,1] neg_lo:[1,0,0] neg_hi:[1,0,0]
	v_pk_fma_f32 v[124:125], v[150:151], v[124:125], v[152:153] op_sel_hi:[1,0,1] neg_lo:[1,0,0] neg_hi:[1,0,0]
	v_pk_mul_f32 v[132:133], v[128:129], v[128:129]
	ds_write_b8 v120, v121 offset:51424
	v_pk_mul_f32 v[150:151], v[124:125], v[124:125]
	v_add_f32_e32 v121, v132, v133
	v_add_f32_e32 v121, v121, v150
	v_add_f32_e32 v121, v121, v151
	s_nop 1
	v_mov_b32_dpp v122, v121 quad_perm:[1,0,3,2] row_mask:0xf bank_mask:0xf
	s_waitcnt lgkmcnt(0)
	v_add_f32_e32 v121, v121, v122
	s_nop 1
	v_mov_b32_dpp v122, v121 quad_perm:[2,3,0,1] row_mask:0xf bank_mask:0xf
	s_waitcnt lgkmcnt(0)
	v_add_f32_e32 v121, v121, v122
	s_nop 1
	v_mov_b32_dpp v122, v121 row_half_mirror row_mask:0xf bank_mask:0xf
	s_nop 1
	v_mov_b32_dpp v122, v122 quad_perm:[3,2,1,0] row_mask:0xf bank_mask:0xf
	s_waitcnt lgkmcnt(0)
	v_add_f32_e32 v121, v121, v122
	s_nop 1
	v_mov_b32_dpp v122, v121 row_ror:8 row_mask:0xf bank_mask:0xf
	s_waitcnt lgkmcnt(0)
	v_add_f32_e32 v121, v121, v122
	ds_swizzle_b32 v122, v121 offset:swizzle(SWAP,16)
	s_waitcnt lgkmcnt(0)
	v_add_f32_e32 v121, v121, v122
	v_mov_b32_e32 v122, s0
	v_fmac_f32_e32 v122, 0x3c000000, v121
	v_cmp_gt_f32_e32 vcc, s1, v122
	v_mul_f32_e32 v121, 0x4b800000, v122
	s_mov_b32 s0, 0x3727c5ac
	v_cndmask_b32_e32 v121, v122, v121, vcc
	v_rsq_f32_e32 v121, v121
	s_nop 0
	v_mul_f32_e32 v122, 0x45800000, v121
	v_cndmask_b32_e32 v121, v121, v122, vcc
	v_mul_f32_e32 v121, v214, v121
	v_mul_f32_e32 v122, v128, v121
	v_mul_f32_e32 v126, v129, v121
	v_mul_f32_e32 v122, v149, v122
	v_mul_f32_e32 v126, v148, v126
	v_mul_f32_e32 v124, v124, v121
	v_mul_f32_e32 v121, v125, v121
	v_mov_b32_e32 v125, v201
	v_cvt_pk_fp8_f32 v125, v122, v126
	v_mul_f32_e32 v124, v147, v124
	v_mul_f32_e32 v121, v146, v121
	v_mul_f32_e32 v122, v213, v143
	v_cvt_pk_fp8_f32 v125, v124, v121 op_sel:[0,0,1]
	v_mov_b32_e32 v124, v67
	v_mov_b32_e32 v126, v123
	v_mov_b32_e32 v128, v35
	v_lshrrev_b32_e32 v121, 8, v125
	ds_write_b8 v120, v125 offset:51456
	ds_write_b8 v120, v121 offset:51488
	ds_write_b8_d16_hi v120, v125 offset:51520
	v_lshrrev_b32_e32 v121, 24, v125
	v_mov_b32_e32 v125, v51
	v_pk_fma_f32 v[124:125], v[124:125], v[122:123], v[126:127] op_sel_hi:[1,0,1] neg_lo:[1,0,0] neg_hi:[1,0,0]
	v_mov_b32_e32 v129, v19
	v_pk_mul_f32 v[126:127], v[124:125], v[124:125]
	v_pk_fma_f32 v[122:123], v[128:129], v[122:123], v[134:135] op_sel_hi:[1,0,1] neg_lo:[1,0,0] neg_hi:[1,0,0]
	ds_write_b8 v120, v121 offset:51552
	v_pk_mul_f32 v[128:129], v[122:123], v[122:123]
	v_add_f32_e32 v121, v126, v127
	v_add_f32_e32 v121, v121, v128
	v_add_f32_e32 v121, v121, v129
	s_nop 1
	v_mov_b32_dpp v126, v121 quad_perm:[1,0,3,2] row_mask:0xf bank_mask:0xf
	s_waitcnt lgkmcnt(0)
	v_add_f32_e32 v121, v121, v126
	s_nop 1
	v_mov_b32_dpp v126, v121 quad_perm:[2,3,0,1] row_mask:0xf bank_mask:0xf
	s_waitcnt lgkmcnt(0)
	v_add_f32_e32 v121, v121, v126
	s_nop 1
	v_mov_b32_dpp v126, v121 row_half_mirror row_mask:0xf bank_mask:0xf
	s_nop 1
	v_mov_b32_dpp v126, v126 quad_perm:[3,2,1,0] row_mask:0xf bank_mask:0xf
	s_waitcnt lgkmcnt(0)
	v_add_f32_e32 v121, v121, v126
	s_nop 1
	v_mov_b32_dpp v126, v121 row_ror:8 row_mask:0xf bank_mask:0xf
	s_waitcnt lgkmcnt(0)
	v_add_f32_e32 v121, v121, v126
	ds_swizzle_b32 v126, v121 offset:swizzle(SWAP,16)
	s_waitcnt lgkmcnt(0)
	v_add_f32_e32 v121, v121, v126
	v_mov_b32_e32 v126, s0
	v_fmac_f32_e32 v126, 0x3c000000, v121
	v_cmp_gt_f32_e32 vcc, s1, v126
	v_mul_f32_e32 v121, 0x4b800000, v126
	s_nop 0
	v_cndmask_b32_e32 v121, v126, v121, vcc
	v_rsq_f32_e32 v121, v121
	s_nop 0
	v_mul_f32_e32 v126, 0x45800000, v121
	v_cndmask_b32_e32 v121, v121, v126, vcc
	v_mul_f32_e32 v121, v214, v121
	v_mul_f32_e32 v124, v124, v121
	v_mul_f32_e32 v125, v125, v121
	v_mul_f32_e32 v124, v149, v124
	v_mul_f32_e32 v125, v148, v125
	v_mul_f32_e32 v122, v122, v121
	v_mul_f32_e32 v121, v123, v121
	v_mov_b32_e32 v123, v201
	v_cvt_pk_fp8_f32 v123, v124, v125
	v_mul_f32_e32 v122, v147, v122
	v_mul_f32_e32 v121, v146, v121
	v_cvt_pk_fp8_f32 v123, v122, v121 op_sel:[0,0,1]
	s_nop 0
	v_lshrrev_b32_e32 v121, 8, v123
	ds_write_b8 v120, v123 offset:51584
	ds_write_b8 v120, v121 offset:51616
	ds_write_b8_d16_hi v120, v123 offset:51648
	v_lshrrev_b32_e32 v121, 24, v123
	ds_write_b8 v120, v121 offset:51680
	v_mul_f32_e32 v122, v213, v140
	v_mov_b32_e32 v124, v68
	v_mov_b32_e32 v125, v52
	v_mov_b32_e32 v126, v104
	v_mov_b32_e32 v127, v108
	v_pk_fma_f32 v[124:125], v[124:125], v[122:123], v[126:127] op_sel_hi:[1,0,1] neg_lo:[1,0,0] neg_hi:[1,0,0]
	v_mov_b32_e32 v128, v36
	v_mov_b32_e32 v129, v20
	v_mov_b32_e32 v130, v112
	v_mov_b32_e32 v131, v116
	v_pk_mul_f32 v[126:127], v[124:125], v[124:125]
	v_pk_fma_f32 v[122:123], v[128:129], v[122:123], v[130:131] op_sel_hi:[1,0,1] neg_lo:[1,0,0] neg_hi:[1,0,0]
	v_add_f32_e32 v104, v126, v127
	v_pk_mul_f32 v[128:129], v[122:123], v[122:123]
	s_mov_b32 s0, 0x3727c5ac
	v_add_f32_e32 v104, v104, v128
	v_add_f32_e32 v104, v104, v129
	s_nop 1
	v_mov_b32_dpp v108, v104 quad_perm:[1,0,3,2] row_mask:0xf bank_mask:0xf
	v_mov_b32_e32 v121, v201
	s_waitcnt lgkmcnt(0)
	v_add_f32_e32 v104, v104, v108
	s_nop 1
	v_mov_b32_dpp v108, v104 quad_perm:[2,3,0,1] row_mask:0xf bank_mask:0xf
	s_waitcnt lgkmcnt(0)
	v_add_f32_e32 v104, v104, v108
	s_nop 1
	v_mov_b32_dpp v108, v104 row_half_mirror row_mask:0xf bank_mask:0xf
	s_nop 1
	v_mov_b32_dpp v108, v108 quad_perm:[3,2,1,0] row_mask:0xf bank_mask:0xf
	s_waitcnt lgkmcnt(0)
	v_add_f32_e32 v104, v104, v108
	s_nop 1
	v_mov_b32_dpp v108, v104 row_ror:8 row_mask:0xf bank_mask:0xf
	s_waitcnt lgkmcnt(0)
	v_add_f32_e32 v104, v104, v108
	ds_swizzle_b32 v108, v104 offset:swizzle(SWAP,16)
	s_waitcnt lgkmcnt(0)
	v_add_f32_e32 v104, v104, v108
	v_mov_b32_e32 v108, s0
	v_fmac_f32_e32 v108, 0x3c000000, v104
	v_cmp_gt_f32_e32 vcc, s1, v108
	v_mul_f32_e32 v104, 0x4b800000, v108
	s_mov_b32 s0, 0x3727c5ac
	v_cndmask_b32_e32 v104, v108, v104, vcc
	v_rsq_f32_e32 v104, v104
	s_nop 0
	v_mul_f32_e32 v108, 0x45800000, v104
	v_cndmask_b32_e32 v104, v104, v108, vcc
	v_mul_f32_e32 v104, v214, v104
	v_mul_f32_e32 v108, v124, v104
	v_mul_f32_e32 v112, v125, v104
	v_mul_f32_e32 v108, v149, v108
	v_mul_f32_e32 v112, v148, v112
	v_cvt_pk_fp8_f32 v121, v108, v112
	v_mul_f32_e32 v116, v122, v104
	v_mul_f32_e32 v104, v123, v104
	v_mul_f32_e32 v116, v147, v116
	v_mul_f32_e32 v104, v146, v104
	v_cvt_pk_fp8_f32 v121, v116, v104 op_sel:[0,0,1]
	v_mov_b32_e32 v122, v69
	v_mov_b32_e32 v123, v53
	v_mov_b32_e32 v108, v105
	v_lshrrev_b32_e32 v104, 8, v121
	ds_write_b8 v120, v121 offset:52224
	ds_write_b8 v120, v104 offset:52256
	ds_write_b8_d16_hi v120, v121 offset:52288
	v_lshrrev_b32_e32 v104, 24, v121
	ds_write_b8 v120, v104 offset:52320
	v_mul_f32_e32 v104, v213, v141
	v_pk_fma_f32 v[108:109], v[122:123], v[104:105], v[108:109] op_sel_hi:[1,0,1] neg_lo:[1,0,0] neg_hi:[1,0,0]
	v_mov_b32_e32 v124, v37
	v_mov_b32_e32 v125, v21
	v_mov_b32_e32 v116, v113
	v_pk_mul_f32 v[122:123], v[108:109], v[108:109]
	v_pk_fma_f32 v[104:105], v[124:125], v[104:105], v[116:117] op_sel_hi:[1,0,1] neg_lo:[1,0,0] neg_hi:[1,0,0]
	v_add_f32_e32 v116, v122, v123
	v_pk_mul_f32 v[112:113], v[104:105], v[104:105]
	v_mov_b32_e32 v117, v22
	v_add_f32_e32 v112, v116, v112
	v_add_f32_e32 v112, v112, v113
	s_nop 1
	v_mov_b32_dpp v113, v112 quad_perm:[1,0,3,2] row_mask:0xf bank_mask:0xf
	v_mov_b32_e32 v116, v38
	v_mov_b32_e32 v122, v114
	v_mov_b32_e32 v123, v118
	v_mov_b32_e32 v118, v115
	s_waitcnt lgkmcnt(0)
	v_add_f32_e32 v112, v112, v113
	s_nop 1
	v_mov_b32_dpp v113, v112 quad_perm:[2,3,0,1] row_mask:0xf bank_mask:0xf
	s_waitcnt lgkmcnt(0)
	v_add_f32_e32 v112, v112, v113
	s_nop 1
	v_mov_b32_dpp v113, v112 row_half_mirror row_mask:0xf bank_mask:0xf
	s_nop 1
	v_mov_b32_dpp v113, v113 quad_perm:[3,2,1,0] row_mask:0xf bank_mask:0xf
	s_waitcnt lgkmcnt(0)
	v_add_f32_e32 v112, v112, v113
	s_nop 1
	v_mov_b32_dpp v113, v112 row_ror:8 row_mask:0xf bank_mask:0xf
	s_waitcnt lgkmcnt(0)
	v_add_f32_e32 v112, v112, v113
	ds_swizzle_b32 v113, v112 offset:swizzle(SWAP,16)
	s_waitcnt lgkmcnt(0)
	v_add_f32_e32 v112, v112, v113
	v_mov_b32_e32 v113, s0
	v_fmac_f32_e32 v113, 0x3c000000, v112
	v_cmp_gt_f32_e32 vcc, s1, v113
	v_mul_f32_e32 v112, 0x4b800000, v113
	s_mov_b32 s0, 0x3727c5ac
	v_cndmask_b32_e32 v112, v113, v112, vcc
	v_rsq_f32_e32 v112, v112
	s_nop 0
	v_mul_f32_e32 v113, 0x45800000, v112
	v_cndmask_b32_e32 v112, v112, v113, vcc
	v_mul_f32_e32 v112, v214, v112
	v_mul_f32_e32 v108, v108, v112
	v_mul_f32_e32 v109, v109, v112
	v_mul_f32_e32 v108, v149, v108
	v_mul_f32_e32 v109, v148, v109
	v_mul_f32_e32 v104, v104, v112
	v_mul_f32_e32 v105, v105, v112
	v_mov_b32_e32 v112, v201
	v_cvt_pk_fp8_f32 v112, v108, v109
	v_mul_f32_e32 v104, v147, v104
	v_mul_f32_e32 v105, v146, v105
	v_mov_b32_e32 v108, v70
	v_cvt_pk_fp8_f32 v112, v104, v105 op_sel:[0,0,1]
	v_mov_b32_e32 v109, v54
	v_mov_b32_e32 v113, v110
	v_lshrrev_b32_e32 v104, 8, v112
	ds_write_b8 v120, v112 offset:52352
	ds_write_b8 v120, v104 offset:52384
	ds_write_b8_d16_hi v120, v112 offset:52416
	v_lshrrev_b32_e32 v104, 24, v112
	ds_write_b8 v120, v104 offset:52448
	v_mul_f32_e32 v104, v213, v138
	v_mov_b32_e32 v112, v106
	v_pk_fma_f32 v[108:109], v[108:109], v[104:105], v[112:113] op_sel_hi:[1,0,1] neg_lo:[1,0,0] neg_hi:[1,0,0]
	v_pk_fma_f32 v[104:105], v[116:117], v[104:105], v[122:123] op_sel_hi:[1,0,1] neg_lo:[1,0,0] neg_hi:[1,0,0]
	v_pk_mul_f32 v[112:113], v[108:109], v[108:109]
	v_pk_mul_f32 v[116:117], v[104:105], v[104:105]
	v_add_f32_e32 v106, v112, v113
	v_add_f32_e32 v106, v106, v116
	v_add_f32_e32 v106, v106, v117
	s_nop 1
	v_mov_b32_dpp v110, v106 quad_perm:[1,0,3,2] row_mask:0xf bank_mask:0xf
	s_waitcnt lgkmcnt(0)
	v_add_f32_e32 v106, v106, v110
	s_nop 1
	v_mov_b32_dpp v110, v106 quad_perm:[2,3,0,1] row_mask:0xf bank_mask:0xf
	s_waitcnt lgkmcnt(0)
	v_add_f32_e32 v106, v106, v110
	s_nop 1
	v_mov_b32_dpp v110, v106 row_half_mirror row_mask:0xf bank_mask:0xf
	s_nop 1
	v_mov_b32_dpp v110, v110 quad_perm:[3,2,1,0] row_mask:0xf bank_mask:0xf
	s_waitcnt lgkmcnt(0)
	v_add_f32_e32 v106, v106, v110
	s_nop 1
	v_mov_b32_dpp v110, v106 row_ror:8 row_mask:0xf bank_mask:0xf
	s_waitcnt lgkmcnt(0)
	v_add_f32_e32 v106, v106, v110
	ds_swizzle_b32 v110, v106 offset:swizzle(SWAP,16)
	s_waitcnt lgkmcnt(0)
	v_add_f32_e32 v106, v106, v110
	v_mov_b32_e32 v110, s0
	v_fmac_f32_e32 v110, 0x3c000000, v106
	v_cmp_gt_f32_e32 vcc, s1, v110
	v_mul_f32_e32 v106, 0x4b800000, v110
	s_mov_b32 s0, 0x3727c5ac
	v_cndmask_b32_e32 v106, v110, v106, vcc
	v_rsq_f32_e32 v106, v106
	s_nop 0
	v_mul_f32_e32 v110, 0x45800000, v106
	v_cndmask_b32_e32 v106, v106, v110, vcc
	v_mul_f32_e32 v106, v214, v106
	v_mul_f32_e32 v108, v108, v106
	v_mul_f32_e32 v109, v109, v106
	v_mul_f32_e32 v108, v149, v108
	v_mul_f32_e32 v109, v148, v109
	v_mul_f32_e32 v104, v104, v106
	v_mul_f32_e32 v105, v105, v106
	v_mov_b32_e32 v106, v201
	v_cvt_pk_fp8_f32 v106, v108, v109
	v_mul_f32_e32 v104, v147, v104
	v_mul_f32_e32 v105, v146, v105
	v_mov_b32_e32 v108, v71
	v_cvt_pk_fp8_f32 v106, v104, v105 op_sel:[0,0,1]
	v_mov_b32_e32 v109, v55
	v_mov_b32_e32 v110, v107
	v_lshrrev_b32_e32 v104, 8, v106
	ds_write_b8 v120, v106 offset:52480
	ds_write_b8 v120, v104 offset:52512
	ds_write_b8_d16_hi v120, v106 offset:52544
	v_lshrrev_b32_e32 v104, 24, v106
	ds_write_b8 v120, v104 offset:52576
	v_mul_f32_e32 v104, v213, v139
	v_pk_fma_f32 v[106:107], v[108:109], v[104:105], v[110:111] op_sel_hi:[1,0,1] neg_lo:[1,0,0] neg_hi:[1,0,0]
	v_mov_b32_e32 v110, v39
	v_mov_b32_e32 v111, v23
	v_pk_mul_f32 v[108:109], v[106:107], v[106:107]
	v_pk_fma_f32 v[104:105], v[110:111], v[104:105], v[118:119] op_sel_hi:[1,0,1] neg_lo:[1,0,0] neg_hi:[1,0,0]
	v_add_f32_e32 v108, v108, v109
	v_pk_mul_f32 v[110:111], v[104:105], v[104:105]
	s_nop 0
	v_add_f32_e32 v108, v108, v110
	v_add_f32_e32 v108, v108, v111
	s_nop 1
	v_mov_b32_dpp v109, v108 quad_perm:[1,0,3,2] row_mask:0xf bank_mask:0xf
	s_waitcnt lgkmcnt(0)
	v_add_f32_e32 v108, v108, v109
	s_nop 1
	v_mov_b32_dpp v109, v108 quad_perm:[2,3,0,1] row_mask:0xf bank_mask:0xf
	s_waitcnt lgkmcnt(0)
	v_add_f32_e32 v108, v108, v109
	s_nop 1
	v_mov_b32_dpp v109, v108 row_half_mirror row_mask:0xf bank_mask:0xf
	s_nop 1
	v_mov_b32_dpp v109, v109 quad_perm:[3,2,1,0] row_mask:0xf bank_mask:0xf
	s_waitcnt lgkmcnt(0)
	v_add_f32_e32 v108, v108, v109
	s_nop 1
	v_mov_b32_dpp v109, v108 row_ror:8 row_mask:0xf bank_mask:0xf
	s_waitcnt lgkmcnt(0)
	v_add_f32_e32 v108, v108, v109
	ds_swizzle_b32 v109, v108 offset:swizzle(SWAP,16)
	s_waitcnt lgkmcnt(0)
	v_add_f32_e32 v108, v108, v109
	v_mov_b32_e32 v109, s0
	v_fmac_f32_e32 v109, 0x3c000000, v108
	v_cmp_gt_f32_e32 vcc, s1, v109
	v_mul_f32_e32 v108, 0x4b800000, v109
	s_nop 0
	v_cndmask_b32_e32 v108, v109, v108, vcc
	v_rsq_f32_e32 v108, v108
	s_nop 0
	v_mul_f32_e32 v109, 0x45800000, v108
	v_cndmask_b32_e32 v108, v108, v109, vcc
	v_mul_f32_e32 v108, v214, v108
	v_mul_f32_e32 v106, v106, v108
	v_mul_f32_e32 v107, v107, v108
	v_mul_f32_e32 v106, v149, v106
	v_mul_f32_e32 v107, v148, v107
	v_mul_f32_e32 v104, v104, v108
	v_mul_f32_e32 v105, v105, v108
	v_mov_b32_e32 v108, v201
	v_cvt_pk_fp8_f32 v108, v106, v107
	v_mul_f32_e32 v104, v147, v104
	v_mul_f32_e32 v105, v146, v105
	v_cvt_pk_fp8_f32 v108, v104, v105 op_sel:[0,0,1]
	s_nop 0
	v_lshrrev_b32_e32 v104, 8, v108
	ds_write_b8 v120, v108 offset:52608
	ds_write_b8 v120, v104 offset:52640
	ds_write_b8_d16_hi v120, v108 offset:52672
	v_lshrrev_b32_e32 v104, 24, v108
	ds_write_b8 v120, v104 offset:52704
	v_rcp_f32_e32 v104, v8
	v_mov_b32_e32 v106, v72
	v_mov_b32_e32 v107, v56
	v_mov_b32_e32 v108, v88
	v_mul_f32_e32 v104, v213, v104
	v_mov_b32_e32 v109, v92
	v_pk_fma_f32 v[106:107], v[106:107], v[104:105], v[108:109] op_sel_hi:[1,0,1] neg_lo:[1,0,0] neg_hi:[1,0,0]
	v_mov_b32_e32 v110, v40
	v_mov_b32_e32 v111, v24
	v_mov_b32_e32 v112, v96
	v_mov_b32_e32 v113, v100
	v_pk_mul_f32 v[108:109], v[106:107], v[106:107]
	v_pk_fma_f32 v[104:105], v[110:111], v[104:105], v[112:113] op_sel_hi:[1,0,1] neg_lo:[1,0,0] neg_hi:[1,0,0]
	v_add_f32_e32 v88, v108, v109
	v_pk_mul_f32 v[110:111], v[104:105], v[104:105]
	s_mov_b32 s0, 0x3727c5ac
	v_add_f32_e32 v88, v88, v110
	v_add_f32_e32 v88, v88, v111
	s_nop 1
	v_mov_b32_dpp v92, v88 quad_perm:[1,0,3,2] row_mask:0xf bank_mask:0xf
	s_waitcnt lgkmcnt(0)
	v_add_f32_e32 v88, v88, v92
	s_nop 1
	v_mov_b32_dpp v92, v88 quad_perm:[2,3,0,1] row_mask:0xf bank_mask:0xf
	s_waitcnt lgkmcnt(0)
	v_add_f32_e32 v88, v88, v92
	s_nop 1
	v_mov_b32_dpp v92, v88 row_half_mirror row_mask:0xf bank_mask:0xf
	s_nop 1
	v_mov_b32_dpp v92, v92 quad_perm:[3,2,1,0] row_mask:0xf bank_mask:0xf
	s_waitcnt lgkmcnt(0)
	v_add_f32_e32 v88, v88, v92
	s_nop 1
	v_mov_b32_dpp v92, v88 row_ror:8 row_mask:0xf bank_mask:0xf
	s_waitcnt lgkmcnt(0)
	v_add_f32_e32 v88, v88, v92
	ds_swizzle_b32 v92, v88 offset:swizzle(SWAP,16)
	s_waitcnt lgkmcnt(0)
	v_add_f32_e32 v88, v88, v92
	v_mov_b32_e32 v92, s0
	v_fmac_f32_e32 v92, 0x3c000000, v88
	v_cmp_gt_f32_e32 vcc, s1, v92
	v_mul_f32_e32 v88, 0x4b800000, v92
	s_mov_b32 s0, 0x3727c5ac
	v_cndmask_b32_e32 v88, v92, v88, vcc
	v_rsq_f32_e32 v88, v88
	s_nop 0
	v_mul_f32_e32 v92, 0x45800000, v88
	v_cndmask_b32_e32 v88, v88, v92, vcc
	v_mul_f32_e32 v88, v214, v88
	v_mul_f32_e32 v92, v106, v88
	v_mul_f32_e32 v96, v107, v88
	v_mul_f32_e32 v92, v149, v92
	v_mul_f32_e32 v96, v148, v96
	v_mul_f32_e32 v100, v104, v88
	v_mov_b32_e32 v104, v201
	v_cvt_pk_fp8_f32 v104, v92, v96
	v_mul_f32_e32 v88, v105, v88
	v_mul_f32_e32 v100, v147, v100
	v_mul_f32_e32 v88, v146, v88
	v_cvt_pk_fp8_f32 v104, v100, v88 op_sel:[0,0,1]
	v_mov_b32_e32 v105, v57
	v_mov_b32_e32 v92, v89
	v_mov_b32_e32 v106, v41
	v_lshrrev_b32_e32 v88, 8, v104
	ds_write_b8 v120, v104 offset:53248
	ds_write_b8 v120, v88 offset:53280
	ds_write_b8_d16_hi v120, v104 offset:53312
	v_lshrrev_b32_e32 v88, 24, v104
	ds_write_b8 v120, v88 offset:53344
	v_rcp_f32_e32 v88, v9
	v_mov_b32_e32 v104, v73
	v_mov_b32_e32 v107, v25
	v_mov_b32_e32 v100, v97
	v_mul_f32_e32 v88, v213, v88
	v_pk_fma_f32 v[92:93], v[104:105], v[88:89], v[92:93] op_sel_hi:[1,0,1] neg_lo:[1,0,0] neg_hi:[1,0,0]
	v_pk_fma_f32 v[88:89], v[106:107], v[88:89], v[100:101] op_sel_hi:[1,0,1] neg_lo:[1,0,0] neg_hi:[1,0,0]
	v_pk_mul_f32 v[104:105], v[92:93], v[92:93]
	v_pk_mul_f32 v[96:97], v[88:89], v[88:89]
	v_add_f32_e32 v100, v104, v105
	v_add_f32_e32 v96, v100, v96
	v_add_f32_e32 v96, v96, v97
	s_nop 1
	v_mov_b32_dpp v97, v96 quad_perm:[1,0,3,2] row_mask:0xf bank_mask:0xf
	v_mov_b32_e32 v100, v42
	v_mov_b32_e32 v101, v26
	v_mov_b32_e32 v104, v98
	s_waitcnt lgkmcnt(0)
	v_add_f32_e32 v96, v96, v97
	s_nop 1
	v_mov_b32_dpp v97, v96 quad_perm:[2,3,0,1] row_mask:0xf bank_mask:0xf
	v_mov_b32_e32 v105, v102
	v_mov_b32_e32 v102, v99
	s_waitcnt lgkmcnt(0)
	v_add_f32_e32 v96, v96, v97
	s_nop 1
	v_mov_b32_dpp v97, v96 row_half_mirror row_mask:0xf bank_mask:0xf
	s_nop 1
	v_mov_b32_dpp v97, v97 quad_perm:[3,2,1,0] row_mask:0xf bank_mask:0xf
	s_waitcnt lgkmcnt(0)
	v_add_f32_e32 v96, v96, v97
	s_nop 1
	v_mov_b32_dpp v97, v96 row_ror:8 row_mask:0xf bank_mask:0xf
	s_waitcnt lgkmcnt(0)
	v_add_f32_e32 v96, v96, v97
	ds_swizzle_b32 v97, v96 offset:swizzle(SWAP,16)
	s_waitcnt lgkmcnt(0)
	v_add_f32_e32 v96, v96, v97
	v_mov_b32_e32 v97, s0
	v_fmac_f32_e32 v97, 0x3c000000, v96
	v_cmp_gt_f32_e32 vcc, s1, v97
	v_mul_f32_e32 v96, 0x4b800000, v97
	s_mov_b32 s0, 0x3727c5ac
	v_cndmask_b32_e32 v96, v97, v96, vcc
	v_rsq_f32_e32 v96, v96
	s_nop 0
	v_mul_f32_e32 v97, 0x45800000, v96
	v_cndmask_b32_e32 v96, v96, v97, vcc
	v_mul_f32_e32 v96, v214, v96
	v_mul_f32_e32 v92, v92, v96
	v_mul_f32_e32 v93, v93, v96
	v_mul_f32_e32 v92, v149, v92
	v_mul_f32_e32 v93, v148, v93
	v_mul_f32_e32 v88, v88, v96
	v_mul_f32_e32 v89, v89, v96
	v_mov_b32_e32 v96, v201
	v_cvt_pk_fp8_f32 v96, v92, v93
	v_mul_f32_e32 v88, v147, v88
	v_mul_f32_e32 v89, v146, v89
	v_mov_b32_e32 v92, v74
	v_cvt_pk_fp8_f32 v96, v88, v89 op_sel:[0,0,1]
	v_mov_b32_e32 v93, v58
	v_mov_b32_e32 v97, v94
	v_lshrrev_b32_e32 v88, 8, v96
	ds_write_b8 v120, v96 offset:53376
	ds_write_b8 v120, v88 offset:53408
	ds_write_b8_d16_hi v120, v96 offset:53440
	v_lshrrev_b32_e32 v88, 24, v96
	ds_write_b8 v120, v88 offset:53472
	v_rcp_f32_e32 v88, v10
	v_mov_b32_e32 v96, v90
	v_mul_f32_e32 v88, v213, v88
	v_pk_fma_f32 v[92:93], v[92:93], v[88:89], v[96:97] op_sel_hi:[1,0,1] neg_lo:[1,0,0] neg_hi:[1,0,0]
	v_pk_fma_f32 v[88:89], v[100:101], v[88:89], v[104:105] op_sel_hi:[1,0,1] neg_lo:[1,0,0] neg_hi:[1,0,0]
	v_pk_mul_f32 v[96:97], v[92:93], v[92:93]
	v_pk_mul_f32 v[100:101], v[88:89], v[88:89]
	v_add_f32_e32 v90, v96, v97
	v_add_f32_e32 v90, v90, v100
	v_add_f32_e32 v90, v90, v101
	s_nop 1
	v_mov_b32_dpp v94, v90 quad_perm:[1,0,3,2] row_mask:0xf bank_mask:0xf
	s_waitcnt lgkmcnt(0)
	v_add_f32_e32 v90, v90, v94
	s_nop 1
	v_mov_b32_dpp v94, v90 quad_perm:[2,3,0,1] row_mask:0xf bank_mask:0xf
	s_waitcnt lgkmcnt(0)
	v_add_f32_e32 v90, v90, v94
	s_nop 1
	v_mov_b32_dpp v94, v90 row_half_mirror row_mask:0xf bank_mask:0xf
	s_nop 1
	v_mov_b32_dpp v94, v94 quad_perm:[3,2,1,0] row_mask:0xf bank_mask:0xf
	s_waitcnt lgkmcnt(0)
	v_add_f32_e32 v90, v90, v94
	s_nop 1
	v_mov_b32_dpp v94, v90 row_ror:8 row_mask:0xf bank_mask:0xf
	s_waitcnt lgkmcnt(0)
	v_add_f32_e32 v90, v90, v94
	ds_swizzle_b32 v94, v90 offset:swizzle(SWAP,16)
	s_waitcnt lgkmcnt(0)
	v_add_f32_e32 v90, v90, v94
	v_mov_b32_e32 v94, s0
	v_fmac_f32_e32 v94, 0x3c000000, v90
	v_cmp_gt_f32_e32 vcc, s1, v94
	v_mul_f32_e32 v90, 0x4b800000, v94
	s_mov_b32 s0, 0x3727c5ac
	v_cndmask_b32_e32 v90, v94, v90, vcc
	v_rsq_f32_e32 v90, v90
	s_nop 0
	v_mul_f32_e32 v94, 0x45800000, v90
	v_cndmask_b32_e32 v90, v90, v94, vcc
	v_mul_f32_e32 v90, v214, v90
	v_mul_f32_e32 v92, v92, v90
	v_mul_f32_e32 v93, v93, v90
	v_mul_f32_e32 v92, v149, v92
	v_mul_f32_e32 v93, v148, v93
	v_mul_f32_e32 v88, v88, v90
	v_mul_f32_e32 v89, v89, v90
	v_mov_b32_e32 v90, v201
	v_cvt_pk_fp8_f32 v90, v92, v93
	v_mul_f32_e32 v88, v147, v88
	v_mul_f32_e32 v89, v146, v89
	v_mov_b32_e32 v92, v75
	v_cvt_pk_fp8_f32 v90, v88, v89 op_sel:[0,0,1]
	v_mov_b32_e32 v93, v59
	v_mov_b32_e32 v94, v91
	v_lshrrev_b32_e32 v88, 8, v90
	ds_write_b8 v120, v90 offset:53504
	ds_write_b8 v120, v88 offset:53536
	ds_write_b8_d16_hi v120, v90 offset:53568
	v_lshrrev_b32_e32 v88, 24, v90
	ds_write_b8 v120, v88 offset:53600
	v_rcp_f32_e32 v88, v11
	s_nop 0
	v_mul_f32_e32 v88, v213, v88
	v_pk_fma_f32 v[90:91], v[92:93], v[88:89], v[94:95] op_sel_hi:[1,0,1] neg_lo:[1,0,0] neg_hi:[1,0,0]
	v_mov_b32_e32 v94, v43
	v_mov_b32_e32 v95, v27
	v_pk_mul_f32 v[92:93], v[90:91], v[90:91]
	v_pk_fma_f32 v[88:89], v[94:95], v[88:89], v[102:103] op_sel_hi:[1,0,1] neg_lo:[1,0,0] neg_hi:[1,0,0]
	v_add_f32_e32 v92, v92, v93
	v_pk_mul_f32 v[94:95], v[88:89], v[88:89]
	s_nop 0
	v_add_f32_e32 v92, v92, v94
	v_add_f32_e32 v92, v92, v95
	s_nop 1
	v_mov_b32_dpp v93, v92 quad_perm:[1,0,3,2] row_mask:0xf bank_mask:0xf
	s_waitcnt lgkmcnt(0)
	v_add_f32_e32 v92, v92, v93
	s_nop 1
	v_mov_b32_dpp v93, v92 quad_perm:[2,3,0,1] row_mask:0xf bank_mask:0xf
	s_waitcnt lgkmcnt(0)
	v_add_f32_e32 v92, v92, v93
	s_nop 1
	v_mov_b32_dpp v93, v92 row_half_mirror row_mask:0xf bank_mask:0xf
	s_nop 1
	v_mov_b32_dpp v93, v93 quad_perm:[3,2,1,0] row_mask:0xf bank_mask:0xf
	s_waitcnt lgkmcnt(0)
	v_add_f32_e32 v92, v92, v93
	s_nop 1
	v_mov_b32_dpp v93, v92 row_ror:8 row_mask:0xf bank_mask:0xf
	s_waitcnt lgkmcnt(0)
	v_add_f32_e32 v92, v92, v93
	ds_swizzle_b32 v93, v92 offset:swizzle(SWAP,16)
	s_waitcnt lgkmcnt(0)
	v_add_f32_e32 v92, v92, v93
	v_mov_b32_e32 v93, s0
	v_fmac_f32_e32 v93, 0x3c000000, v92
	v_cmp_gt_f32_e32 vcc, s1, v93
	v_mul_f32_e32 v92, 0x4b800000, v93
	s_nop 0
	v_cndmask_b32_e32 v92, v93, v92, vcc
	v_rsq_f32_e32 v92, v92
	s_nop 0
	v_mul_f32_e32 v93, 0x45800000, v92
	v_cndmask_b32_e32 v92, v92, v93, vcc
	v_mul_f32_e32 v92, v214, v92
	v_mul_f32_e32 v90, v90, v92
	v_mul_f32_e32 v91, v91, v92
	v_mul_f32_e32 v90, v149, v90
	v_mul_f32_e32 v91, v148, v91
	v_mul_f32_e32 v88, v88, v92
	v_mul_f32_e32 v89, v89, v92
	v_mov_b32_e32 v92, v201
	v_cvt_pk_fp8_f32 v92, v90, v91
	v_mul_f32_e32 v88, v147, v88
	v_mul_f32_e32 v89, v146, v89
	v_cvt_pk_fp8_f32 v92, v88, v89 op_sel:[0,0,1]
	s_nop 0
	v_lshrrev_b32_e32 v88, 8, v92
	ds_write_b8 v120, v92 offset:53632
	ds_write_b8 v120, v88 offset:53664
	ds_write_b8_d16_hi v120, v92 offset:53696
	v_lshrrev_b32_e32 v88, 24, v92
	ds_write_b8 v120, v88 offset:53728
	v_rcp_f32_e32 v88, v12
	v_mov_b32_e32 v90, v76
	v_mov_b32_e32 v91, v60
	v_mov_b32_e32 v92, v0
	v_mul_f32_e32 v88, v213, v88
	v_mov_b32_e32 v93, v4
	v_pk_fma_f32 v[90:91], v[90:91], v[88:89], v[92:93] op_sel_hi:[1,0,1] neg_lo:[1,0,0] neg_hi:[1,0,0]
	v_mov_b32_e32 v94, v44
	v_mov_b32_e32 v95, v28
	v_mov_b32_e32 v96, v80
	v_mov_b32_e32 v97, v84
	v_pk_mul_f32 v[92:93], v[90:91], v[90:91]
	v_pk_fma_f32 v[88:89], v[94:95], v[88:89], v[96:97] op_sel_hi:[1,0,1] neg_lo:[1,0,0] neg_hi:[1,0,0]
	v_add_f32_e32 v0, v92, v93
	v_pk_mul_f32 v[94:95], v[88:89], v[88:89]
	s_mov_b32 s0, 0x3727c5ac
	v_add_f32_e32 v0, v0, v94
	v_add_f32_e32 v0, v0, v95
	s_nop 1
	v_mov_b32_dpp v4, v0 quad_perm:[1,0,3,2] row_mask:0xf bank_mask:0xf
	s_waitcnt lgkmcnt(0)
	v_add_f32_e32 v0, v0, v4
	s_nop 1
	v_mov_b32_dpp v4, v0 quad_perm:[2,3,0,1] row_mask:0xf bank_mask:0xf
	s_waitcnt lgkmcnt(0)
	v_add_f32_e32 v0, v0, v4
	s_nop 1
	v_mov_b32_dpp v4, v0 row_half_mirror row_mask:0xf bank_mask:0xf
	s_nop 1
	v_mov_b32_dpp v4, v4 quad_perm:[3,2,1,0] row_mask:0xf bank_mask:0xf
	s_waitcnt lgkmcnt(0)
	v_add_f32_e32 v0, v0, v4
	s_nop 1
	v_mov_b32_dpp v4, v0 row_ror:8 row_mask:0xf bank_mask:0xf
	s_waitcnt lgkmcnt(0)
	v_add_f32_e32 v0, v0, v4
	ds_swizzle_b32 v4, v0 offset:swizzle(SWAP,16)
	s_waitcnt lgkmcnt(0)
	v_add_f32_e32 v0, v0, v4
	v_mov_b32_e32 v4, s0
	v_fmac_f32_e32 v4, 0x3c000000, v0
	v_cmp_gt_f32_e32 vcc, s1, v4
	v_mul_f32_e32 v0, 0x4b800000, v4
	s_mov_b32 s0, 0x3727c5ac
	v_cndmask_b32_e32 v0, v4, v0, vcc
	v_rsq_f32_e32 v0, v0
	s_nop 0
	v_mul_f32_e32 v4, 0x45800000, v0
	v_cndmask_b32_e32 v0, v0, v4, vcc
	v_mul_f32_e32 v0, v214, v0
	v_mul_f32_e32 v4, v90, v0
	v_mul_f32_e32 v80, v91, v0
	v_mul_f32_e32 v4, v149, v4
	v_mul_f32_e32 v80, v148, v80
	v_mul_f32_e32 v84, v88, v0
	v_mov_b32_e32 v88, v201
	v_cvt_pk_fp8_f32 v88, v4, v80
	v_mul_f32_e32 v0, v89, v0
	v_mul_f32_e32 v84, v147, v84
	v_mul_f32_e32 v0, v146, v0
	v_cvt_pk_fp8_f32 v88, v84, v0 op_sel:[0,0,1]
	v_mov_b32_e32 v89, v61
	v_mov_b32_e32 v4, v1
	v_mov_b32_e32 v90, v45
	v_lshrrev_b32_e32 v0, 8, v88
	ds_write_b8 v120, v88 offset:54272
	ds_write_b8 v120, v0 offset:54304
	ds_write_b8_d16_hi v120, v88 offset:54336
	v_lshrrev_b32_e32 v0, 24, v88
	ds_write_b8 v120, v0 offset:54368
	v_rcp_f32_e32 v0, v13
	v_mov_b32_e32 v88, v77
	v_mov_b32_e32 v91, v29
	v_mov_b32_e32 v84, v81
	v_mul_f32_e32 v0, v213, v0
	v_pk_fma_f32 v[4:5], v[88:89], v[0:1], v[4:5] op_sel_hi:[1,0,1] neg_lo:[1,0,0] neg_hi:[1,0,0]
	v_pk_fma_f32 v[0:1], v[90:91], v[0:1], v[84:85] op_sel_hi:[1,0,1] neg_lo:[1,0,0] neg_hi:[1,0,0]
	v_pk_mul_f32 v[88:89], v[4:5], v[4:5]
	v_pk_mul_f32 v[80:81], v[0:1], v[0:1]
	v_add_f32_e32 v84, v88, v89
	v_add_f32_e32 v80, v84, v80
	v_add_f32_e32 v80, v80, v81
	s_nop 1
	v_mov_b32_dpp v81, v80 quad_perm:[1,0,3,2] row_mask:0xf bank_mask:0xf
	v_mov_b32_e32 v84, v46
	v_mov_b32_e32 v85, v30
	v_mov_b32_e32 v88, v82
	s_waitcnt lgkmcnt(0)
	v_add_f32_e32 v80, v80, v81
	s_nop 1
	v_mov_b32_dpp v81, v80 quad_perm:[2,3,0,1] row_mask:0xf bank_mask:0xf
	v_mov_b32_e32 v89, v86
	v_mov_b32_e32 v86, v83
	s_waitcnt lgkmcnt(0)
	v_add_f32_e32 v80, v80, v81
	s_nop 1
	v_mov_b32_dpp v81, v80 row_half_mirror row_mask:0xf bank_mask:0xf
	s_nop 1
	v_mov_b32_dpp v81, v81 quad_perm:[3,2,1,0] row_mask:0xf bank_mask:0xf
	s_waitcnt lgkmcnt(0)
	v_add_f32_e32 v80, v80, v81
	s_nop 1
	v_mov_b32_dpp v81, v80 row_ror:8 row_mask:0xf bank_mask:0xf
	s_waitcnt lgkmcnt(0)
	v_add_f32_e32 v80, v80, v81
	ds_swizzle_b32 v81, v80 offset:swizzle(SWAP,16)
	s_waitcnt lgkmcnt(0)
	v_add_f32_e32 v80, v80, v81
	v_mov_b32_e32 v81, s0
	v_fmac_f32_e32 v81, 0x3c000000, v80
	v_cmp_gt_f32_e32 vcc, s1, v81
	v_mul_f32_e32 v80, 0x4b800000, v81
	s_mov_b32 s0, 0x3727c5ac
	v_cndmask_b32_e32 v80, v81, v80, vcc
	v_rsq_f32_e32 v80, v80
	s_nop 0
	v_mul_f32_e32 v81, 0x45800000, v80
	v_cndmask_b32_e32 v80, v80, v81, vcc
	v_mul_f32_e32 v80, v214, v80
	v_mul_f32_e32 v4, v4, v80
	v_mul_f32_e32 v5, v5, v80
	v_mul_f32_e32 v4, v149, v4
	v_mul_f32_e32 v5, v148, v5
	v_mul_f32_e32 v0, v0, v80
	v_mul_f32_e32 v1, v1, v80
	v_mov_b32_e32 v80, v201
	v_cvt_pk_fp8_f32 v80, v4, v5
	v_mul_f32_e32 v0, v147, v0
	v_mul_f32_e32 v1, v146, v1
	v_mov_b32_e32 v4, v78
	v_cvt_pk_fp8_f32 v80, v0, v1 op_sel:[0,0,1]
	v_mov_b32_e32 v5, v62
	v_mov_b32_e32 v81, v6
	v_lshrrev_b32_e32 v0, 8, v80
	ds_write_b8 v120, v80 offset:54400
	ds_write_b8 v120, v0 offset:54432
	ds_write_b8_d16_hi v120, v80 offset:54464
	v_lshrrev_b32_e32 v0, 24, v80
	ds_write_b8 v120, v0 offset:54496
	v_rcp_f32_e32 v0, v14
	v_mov_b32_e32 v80, v2
	v_mul_f32_e32 v0, v213, v0
	v_pk_fma_f32 v[4:5], v[4:5], v[0:1], v[80:81] op_sel_hi:[1,0,1] neg_lo:[1,0,0] neg_hi:[1,0,0]
	v_pk_fma_f32 v[0:1], v[84:85], v[0:1], v[88:89] op_sel_hi:[1,0,1] neg_lo:[1,0,0] neg_hi:[1,0,0]
	v_pk_mul_f32 v[80:81], v[4:5], v[4:5]
	v_pk_mul_f32 v[84:85], v[0:1], v[0:1]
	v_add_f32_e32 v2, v80, v81
	v_add_f32_e32 v2, v2, v84
	v_add_f32_e32 v2, v2, v85
	s_nop 1
	v_mov_b32_dpp v6, v2 quad_perm:[1,0,3,2] row_mask:0xf bank_mask:0xf
	s_waitcnt lgkmcnt(0)
	v_add_f32_e32 v2, v2, v6
	s_nop 1
	v_mov_b32_dpp v6, v2 quad_perm:[2,3,0,1] row_mask:0xf bank_mask:0xf
	s_waitcnt lgkmcnt(0)
	v_add_f32_e32 v2, v2, v6
	s_nop 1
	v_mov_b32_dpp v6, v2 row_half_mirror row_mask:0xf bank_mask:0xf
	s_nop 1
	v_mov_b32_dpp v6, v6 quad_perm:[3,2,1,0] row_mask:0xf bank_mask:0xf
	s_waitcnt lgkmcnt(0)
	v_add_f32_e32 v2, v2, v6
	s_nop 1
	v_mov_b32_dpp v6, v2 row_ror:8 row_mask:0xf bank_mask:0xf
	s_waitcnt lgkmcnt(0)
	v_add_f32_e32 v2, v2, v6
	ds_swizzle_b32 v6, v2 offset:swizzle(SWAP,16)
	s_waitcnt lgkmcnt(0)
	v_add_f32_e32 v2, v2, v6
	v_mov_b32_e32 v6, s0
	v_fmac_f32_e32 v6, 0x3c000000, v2
	v_cmp_gt_f32_e32 vcc, s1, v6
	v_mul_f32_e32 v2, 0x4b800000, v6
	s_mov_b32 s0, 0x3727c5ac
	v_cndmask_b32_e32 v2, v6, v2, vcc
	v_rsq_f32_e32 v2, v2
	s_nop 0
	v_mul_f32_e32 v6, 0x45800000, v2
	v_cndmask_b32_e32 v2, v2, v6, vcc
	v_mul_f32_e32 v2, v214, v2
	v_mul_f32_e32 v4, v4, v2
	v_mul_f32_e32 v5, v5, v2
	v_mul_f32_e32 v4, v149, v4
	v_mul_f32_e32 v5, v148, v5
	v_mul_f32_e32 v0, v0, v2
	v_mul_f32_e32 v1, v1, v2
	v_mov_b32_e32 v2, v201
	v_cvt_pk_fp8_f32 v2, v4, v5
	v_mul_f32_e32 v0, v147, v0
	v_mul_f32_e32 v1, v146, v1
	v_mov_b32_e32 v4, v79
	v_cvt_pk_fp8_f32 v2, v0, v1 op_sel:[0,0,1]
	v_mov_b32_e32 v5, v63
	v_mov_b32_e32 v6, v3
	v_lshrrev_b32_e32 v0, 8, v2
	ds_write_b8 v120, v2 offset:54528
	ds_write_b8 v120, v0 offset:54560
	ds_write_b8_d16_hi v120, v2 offset:54592
	v_lshrrev_b32_e32 v0, 24, v2
	ds_write_b8 v120, v0 offset:54624
	v_rcp_f32_e32 v0, v15
	s_nop 0
	v_mul_f32_e32 v0, v213, v0
	v_pk_fma_f32 v[2:3], v[4:5], v[0:1], v[6:7] op_sel_hi:[1,0,1] neg_lo:[1,0,0] neg_hi:[1,0,0]
	v_mov_b32_e32 v6, v47
	v_mov_b32_e32 v7, v31
	v_pk_mul_f32 v[4:5], v[2:3], v[2:3]
	v_pk_fma_f32 v[0:1], v[6:7], v[0:1], v[86:87] op_sel_hi:[1,0,1] neg_lo:[1,0,0] neg_hi:[1,0,0]
	v_add_f32_e32 v4, v4, v5
	v_pk_mul_f32 v[6:7], v[0:1], v[0:1]
	s_nop 0
	v_add_f32_e32 v4, v4, v6
	v_add_f32_e32 v4, v4, v7
	s_nop 1
	v_mov_b32_dpp v5, v4 quad_perm:[1,0,3,2] row_mask:0xf bank_mask:0xf
	s_waitcnt lgkmcnt(0)
	v_add_f32_e32 v4, v4, v5
	s_nop 1
	v_mov_b32_dpp v5, v4 quad_perm:[2,3,0,1] row_mask:0xf bank_mask:0xf
	s_waitcnt lgkmcnt(0)
	v_add_f32_e32 v4, v4, v5
	s_nop 1
	v_mov_b32_dpp v5, v4 row_half_mirror row_mask:0xf bank_mask:0xf
	s_nop 1
	v_mov_b32_dpp v5, v5 quad_perm:[3,2,1,0] row_mask:0xf bank_mask:0xf
	s_waitcnt lgkmcnt(0)
	v_add_f32_e32 v4, v4, v5
	s_nop 1
	v_mov_b32_dpp v5, v4 row_ror:8 row_mask:0xf bank_mask:0xf
	s_waitcnt lgkmcnt(0)
	v_add_f32_e32 v4, v4, v5
	ds_swizzle_b32 v5, v4 offset:swizzle(SWAP,16)
	s_waitcnt lgkmcnt(0)
	v_add_f32_e32 v4, v4, v5
	v_mov_b32_e32 v5, s0
	v_fmac_f32_e32 v5, 0x3c000000, v4
	v_cmp_gt_f32_e32 vcc, s1, v5
	v_mul_f32_e32 v4, 0x4b800000, v5
	s_nop 0
	v_cndmask_b32_e32 v4, v5, v4, vcc
	v_rsq_f32_e32 v4, v4
	s_nop 0
	v_mul_f32_e32 v5, 0x45800000, v4
	v_cndmask_b32_e32 v4, v4, v5, vcc
	v_mul_f32_e32 v4, v214, v4
	v_mul_f32_e32 v2, v2, v4
	v_mul_f32_e32 v3, v3, v4
	v_mul_f32_e32 v2, v149, v2
	v_mul_f32_e32 v3, v148, v3
	v_mul_f32_e32 v0, v0, v4
	v_mul_f32_e32 v1, v1, v4
	v_mov_b32_e32 v4, v201
	v_cvt_pk_fp8_f32 v4, v2, v3
	v_mul_f32_e32 v0, v147, v0
	v_mul_f32_e32 v1, v146, v1
	v_cvt_pk_fp8_f32 v4, v0, v1 op_sel:[0,0,1]
	s_nop 0
	v_lshrrev_b32_e32 v0, 8, v4
	ds_write_b8 v120, v4 offset:54656
	ds_write_b8 v120, v0 offset:54688
	ds_write_b8_d16_hi v120, v4 offset:54720
	v_lshrrev_b32_e32 v0, 24, v4
	ds_write_b8 v120, v0 offset:54752
	v_and_b32_e32 v200, 0x70, v215
	v_add_u32_e32 v80, s89, v200
	v_lshrrev_b32_e32 v81, 3, v216
	s_waitcnt lgkmcnt(0)
	v_lshl_add_u32 v0, v81, 7, v80
	ds_read_b128 v[0:3], v0 offset:51200
	v_lshl_add_u64 v[4:5], s[68:69], 0, v[200:201]
	v_lshlrev_b32_e32 v200, 10, v81
	v_lshl_add_u64 v[6:7], v[4:5], 0, v[200:201]
	s_mov_b64 s[0:1], 0
	s_waitcnt lgkmcnt(0)
	global_store_dwordx4 v[6:7], v[0:3], off
	v_or_b32_e32 v6, 8, v81
	v_lshlrev_b32_e32 v200, 10, v6
	v_lshl_add_u32 v0, v6, 7, v80
	ds_read_b128 v[0:3], v0 offset:51200
	v_lshl_add_u64 v[6:7], v[4:5], 0, v[200:201]
	s_waitcnt lgkmcnt(0)
	global_store_dwordx4 v[6:7], v[0:3], off
	v_or_b32_e32 v6, 16, v81
	s_nop 0
	v_lshl_add_u32 v0, v6, 7, v80
	ds_read_b128 v[0:3], v0 offset:51200
	v_lshlrev_b32_e32 v200, 10, v6
	v_lshl_add_u64 v[6:7], v[4:5], 0, v[200:201]
	s_waitcnt lgkmcnt(0)
	global_store_dwordx4 v[6:7], v[0:3], off
	v_or_b32_e32 v6, 24, v81
	s_nop 0
	v_lshl_add_u32 v0, v6, 7, v80
	ds_read_b128 v[0:3], v0 offset:51200
	v_lshlrev_b32_e32 v200, 10, v6
	v_lshl_add_u64 v[4:5], v[4:5], 0, v[200:201]
	s_waitcnt lgkmcnt(0)
	global_store_dwordx4 v[4:5], v[0:3], off

.LBB0_942:
	v_mbcnt_lo_u32_b32 v128, -1, 0
	v_mbcnt_hi_u32_b32 v128, -1, v128
	v_lshrrev_b32_e32 v129, 1, v128
	v_and_or_b32 v180, v129, 24, s46
	v_lshl_add_u32 v129, v180, 2, s20
	v_and_b32_e32 v181, 15, v128
	s_add_i32 s20, s20, s58
	v_add_u32_e32 v134, 0x20000, v129
	v_add_u32_e32 v129, 0x20400, v129
	v_lshl_add_u32 v128, v181, 2, s20
	ds_read_b128 v[136:139], v134
	ds_read_b128 v[140:143], v134 offset:16
	ds_read_b128 v[144:147], v129
	ds_read_b128 v[148:151], v129 offset:16
	ds_read_b128 v[186:189], v134 offset:512
	ds_read_b128 v[152:155], v129 offset:512
	ds_read_b128 v[190:193], v134 offset:528
	ds_read_b128 v[194:197], v129 offset:528
	v_add_u32_e32 v129, 0x20800, v128
	ds_read2_b32 v[166:167], v129 offset1:16
	ds_read2_b32 v[164:165], v129 offset0:32 offset1:48
	v_add_u32_e32 v128, 0x20a00, v128
	s_mov_b32 s4, 0xc01d265f
	s_mov_b32 s15, 0xc1898193
	s_mov_b32 s17, 0xc1c37b6f
	s_mov_b32 s16, 0xc0437b6f
	s_mov_b32 s14, 0x41929c93
	ds_read2_b32 v[162:163], v128 offset1:16
	ds_read2_b32 v[128:129], v128 offset0:32 offset1:48
	v_lshl_or_b32 v181, v181, 10, s59
	v_or_b32_e32 v182, v181, v180
	v_add_u32_e32 v183, v181, v180
	v_mov_b32_e32 v135, s17
	v_cvt_f32_i32_e32 v120, v120
	v_cvt_f32_i32_e32 v121, v121
	v_cvt_f32_i32_e32 v122, v122
	v_cvt_f32_i32_e32 v123, v123
	v_cvt_f32_i32_e32 v124, v124
	v_cvt_f32_i32_e32 v125, v125
	v_cvt_f32_i32_e32 v126, v126
	v_cvt_f32_i32_e32 v127, v127
	v_cvt_f32_i32_e32 v112, v112
	v_cvt_f32_i32_e32 v113, v113
	v_cvt_f32_i32_e32 v114, v114
	v_cvt_f32_i32_e32 v115, v115
	v_cvt_f32_i32_e32 v116, v116
	v_cvt_f32_i32_e32 v117, v117
	v_cvt_f32_i32_e32 v118, v118
	v_cvt_f32_i32_e32 v119, v119
	s_waitcnt lgkmcnt(0)
	v_pk_mul_f32 v[144:145], v[144:145], s[4:5] op_sel_hi:[1,0]
	v_pk_mul_f32 v[136:137], v[136:137], s[4:5] op_sel_hi:[1,0]
	v_pk_mul_f32 v[152:153], v[152:153], s[16:17] op_sel_hi:[1,0]
	v_pk_fma_f32 v[186:187], v[186:187], s[16:17], s[16:17] op_sel_hi:[1,0,0]
	v_pk_mul_f32 v[146:147], v[146:147], s[4:5] op_sel_hi:[1,0]
	v_pk_mul_f32 v[138:139], v[138:139], s[4:5] op_sel_hi:[1,0]
	v_pk_mul_f32 v[154:155], v[154:155], s[16:17] op_sel_hi:[1,0]
	v_pk_fma_f32 v[188:189], v[188:189], s[16:17], s[16:17] op_sel_hi:[1,0,0]
	v_pk_mul_f32 v[148:149], v[148:149], s[4:5] op_sel_hi:[1,0]
	v_pk_mul_f32 v[140:141], v[140:141], s[4:5] op_sel_hi:[1,0]
	v_pk_mul_f32 v[194:195], v[194:195], s[16:17] op_sel_hi:[1,0]
	v_pk_fma_f32 v[190:191], v[190:191], s[16:17], s[16:17] op_sel_hi:[1,0,0]
	v_pk_mul_f32 v[150:151], v[150:151], s[4:5] op_sel_hi:[1,0]
	v_pk_mul_f32 v[142:143], v[142:143], s[4:5] op_sel_hi:[1,0]
	v_pk_mul_f32 v[196:197], v[196:197], s[16:17] op_sel_hi:[1,0]
	v_pk_fma_f32 v[192:193], v[192:193], s[16:17], s[16:17] op_sel_hi:[1,0,0]
	s_add_u32 s4, s39, s33
	s_addc_u32 s5, s40, 0
	v_pk_mul_f32 v[120:121], v[144:145], v[120:121]
	v_pk_mul_f32 v[122:123], v[146:147], v[122:123]
	v_pk_mul_f32 v[112:113], v[148:149], v[112:113]
	v_pk_mul_f32 v[114:115], v[150:151], v[114:115]
	v_pk_fma_f32 v[120:121], v[166:167], v[120:121], v[136:137] op_sel_hi:[0,1,1]
	v_pk_fma_f32 v[122:123], v[166:167], v[122:123], v[138:139] op_sel_hi:[0,1,1]
	v_pk_fma_f32 v[112:113], v[166:167], v[112:113], v[140:141] op_sel_hi:[0,1,1]
	v_pk_fma_f32 v[114:115], v[166:167], v[114:115], v[142:143] op_sel_hi:[0,1,1]
	v_max_f32_e32 v120, s15, v120
	v_max_f32_e32 v121, s15, v121
	v_max_f32_e32 v122, s15, v122
	v_max_f32_e32 v123, s15, v123
	v_max_f32_e32 v112, s15, v112
	v_max_f32_e32 v113, s15, v113
	v_max_f32_e32 v114, s15, v114
	v_max_f32_e32 v115, s15, v115
	v_exp_f32_e32 v156, v120
	v_exp_f32_e32 v157, v121
	v_exp_f32_e32 v158, v122
	v_exp_f32_e32 v159, v123
	v_exp_f32_e32 v160, v112
	v_exp_f32_e32 v161, v113
	v_exp_f32_e32 v184, v114
	v_exp_f32_e32 v185, v115
	v_pk_mul_f32 v[124:125], v[152:153], v[124:125]
	v_pk_mul_f32 v[126:127], v[154:155], v[126:127]
	v_pk_mul_f32 v[116:117], v[194:195], v[116:117]
	v_pk_mul_f32 v[118:119], v[196:197], v[118:119]
	v_pk_fma_f32 v[124:125], v[166:167], v[124:125], v[186:187] op_sel_hi:[0,1,1]
	v_pk_fma_f32 v[126:127], v[166:167], v[126:127], v[188:189] op_sel_hi:[0,1,1]
	v_pk_fma_f32 v[116:117], v[166:167], v[116:117], v[190:191] op_sel_hi:[0,1,1]
	v_pk_fma_f32 v[118:119], v[166:167], v[118:119], v[192:193] op_sel_hi:[0,1,1]
	v_pk_add_f32 v[156:157], v[156:157], 1.0 op_sel_hi:[1,0]
	v_pk_add_f32 v[158:159], v[158:159], 1.0 op_sel_hi:[1,0]
	v_pk_add_f32 v[160:161], v[160:161], 1.0 op_sel_hi:[1,0]
	v_pk_add_f32 v[184:185], v[184:185], 1.0 op_sel_hi:[1,0]
	v_rcp_f32_e32 v156, v156
	v_rcp_f32_e32 v157, v157
	v_rcp_f32_e32 v158, v158
	v_rcp_f32_e32 v159, v159
	v_rcp_f32_e32 v160, v160
	v_rcp_f32_e32 v161, v161
	v_rcp_f32_e32 v184, v184
	v_rcp_f32_e32 v185, v185
	v_med3_f32 v124, v124, s14, v135
	v_med3_f32 v125, v125, s14, v135
	v_med3_f32 v126, v126, s14, v135
	v_med3_f32 v127, v127, s14, v135
	v_med3_f32 v116, v116, s14, v135
	v_med3_f32 v117, v117, s14, v135
	v_med3_f32 v118, v118, s14, v135
	v_med3_f32 v119, v119, s14, v135
	v_pk_mul_f32 v[156:157], v[120:121], v[156:157]
	v_pk_mul_f32 v[158:159], v[122:123], v[158:159]
	v_pk_mul_f32 v[160:161], v[112:113], v[160:161]
	v_pk_mul_f32 v[184:185], v[114:115], v[184:185]
	v_pk_mul_f32 v[124:125], v[124:125], v[156:157]
	v_pk_mul_f32 v[126:127], v[126:127], v[158:159]
	v_pk_mul_f32 v[116:117], v[116:117], v[160:161]
	v_pk_mul_f32 v[118:119], v[118:119], v[184:185]
	v_cvt_pk_fp8_f32 v130, v124, v125
	v_cvt_pk_fp8_f32 v131, v116, v117
	v_cvt_pk_fp8_f32 v130, v126, v127 op_sel:[0,0,1]
	v_cvt_pk_fp8_f32 v131, v118, v119 op_sel:[0,0,1]
	s_nop 0
	global_store_dwordx2 v182, v[130:131], s[4:5]
	v_cvt_f32_i32_e32 v104, v104
	v_cvt_f32_i32_e32 v105, v105
	v_cvt_f32_i32_e32 v106, v106
	v_cvt_f32_i32_e32 v107, v107
	v_cvt_f32_i32_e32 v96, v96
	v_cvt_f32_i32_e32 v97, v97
	v_cvt_f32_i32_e32 v98, v98
	v_cvt_f32_i32_e32 v99, v99
	v_pk_mul_f32 v[104:105], v[144:145], v[104:105]
	v_pk_mul_f32 v[106:107], v[146:147], v[106:107]
	v_pk_mul_f32 v[96:97], v[148:149], v[96:97]
	v_pk_mul_f32 v[98:99], v[150:151], v[98:99]
	v_pk_fma_f32 v[104:105], v[166:167], v[104:105], v[136:137] op_sel:[1,0,0] op_sel_hi:[1,1,1]
	v_pk_fma_f32 v[106:107], v[166:167], v[106:107], v[138:139] op_sel:[1,0,0] op_sel_hi:[1,1,1]
	v_pk_fma_f32 v[96:97], v[166:167], v[96:97], v[140:141] op_sel:[1,0,0] op_sel_hi:[1,1,1]
	v_pk_fma_f32 v[98:99], v[166:167], v[98:99], v[142:143] op_sel:[1,0,0] op_sel_hi:[1,1,1]
	v_max_f32_e32 v104, s15, v104
	v_max_f32_e32 v105, s15, v105
	v_max_f32_e32 v106, s15, v106
	v_max_f32_e32 v107, s15, v107
	v_max_f32_e32 v96, s15, v96
	v_max_f32_e32 v97, s15, v97
	v_max_f32_e32 v98, s15, v98
	v_max_f32_e32 v99, s15, v99
	v_exp_f32_e32 v156, v104
	v_exp_f32_e32 v157, v105
	v_exp_f32_e32 v158, v106
	v_exp_f32_e32 v159, v107
	v_exp_f32_e32 v160, v96
	v_exp_f32_e32 v161, v97
	v_exp_f32_e32 v184, v98
	v_exp_f32_e32 v185, v99
	v_cvt_f32_i32_e32 v108, v108
	v_cvt_f32_i32_e32 v109, v109
	v_cvt_f32_i32_e32 v110, v110
	v_cvt_f32_i32_e32 v111, v111
	v_cvt_f32_i32_e32 v100, v100
	v_cvt_f32_i32_e32 v101, v101
	v_cvt_f32_i32_e32 v102, v102
	v_cvt_f32_i32_e32 v103, v103
	v_pk_mul_f32 v[108:109], v[152:153], v[108:109]
	v_pk_mul_f32 v[110:111], v[154:155], v[110:111]
	v_pk_mul_f32 v[100:101], v[194:195], v[100:101]
	v_pk_mul_f32 v[102:103], v[196:197], v[102:103]
	v_pk_fma_f32 v[108:109], v[166:167], v[108:109], v[186:187] op_sel:[1,0,0] op_sel_hi:[1,1,1]
	v_pk_fma_f32 v[110:111], v[166:167], v[110:111], v[188:189] op_sel:[1,0,0] op_sel_hi:[1,1,1]
	v_pk_fma_f32 v[100:101], v[166:167], v[100:101], v[190:191] op_sel:[1,0,0] op_sel_hi:[1,1,1]
	v_pk_fma_f32 v[102:103], v[166:167], v[102:103], v[192:193] op_sel:[1,0,0] op_sel_hi:[1,1,1]
	v_pk_add_f32 v[156:157], v[156:157], 1.0 op_sel_hi:[1,0]
	v_pk_add_f32 v[158:159], v[158:159], 1.0 op_sel_hi:[1,0]
	v_pk_add_f32 v[160:161], v[160:161], 1.0 op_sel_hi:[1,0]
	v_pk_add_f32 v[184:185], v[184:185], 1.0 op_sel_hi:[1,0]
	v_rcp_f32_e32 v156, v156
	v_rcp_f32_e32 v157, v157
	v_rcp_f32_e32 v158, v158
	v_rcp_f32_e32 v159, v159
	v_rcp_f32_e32 v160, v160
	v_rcp_f32_e32 v161, v161
	v_rcp_f32_e32 v184, v184
	v_rcp_f32_e32 v185, v185
	v_med3_f32 v108, v108, s14, v135
	v_med3_f32 v109, v109, s14, v135
	v_med3_f32 v110, v110, s14, v135
	v_med3_f32 v111, v111, s14, v135
	v_med3_f32 v100, v100, s14, v135
	v_med3_f32 v101, v101, s14, v135
	v_med3_f32 v102, v102, s14, v135
	v_med3_f32 v103, v103, s14, v135
	v_pk_mul_f32 v[156:157], v[104:105], v[156:157]
	v_pk_mul_f32 v[158:159], v[106:107], v[158:159]
	v_pk_mul_f32 v[160:161], v[96:97], v[160:161]
	v_pk_mul_f32 v[184:185], v[98:99], v[184:185]
	v_pk_mul_f32 v[108:109], v[108:109], v[156:157]
	v_pk_mul_f32 v[110:111], v[110:111], v[158:159]
	v_pk_mul_f32 v[100:101], v[100:101], v[160:161]
	v_pk_mul_f32 v[102:103], v[102:103], v[184:185]
	v_cvt_pk_fp8_f32 v132, v108, v109
	v_cvt_pk_fp8_f32 v133, v100, v101
	v_cvt_pk_fp8_f32 v132, v110, v111 op_sel:[0,0,1]
	v_cvt_pk_fp8_f32 v133, v102, v103 op_sel:[0,0,1]
	v_or_b32_e32 v134, 0x4000, v182
	s_nop 0
	global_store_dwordx2 v134, v[132:133], s[4:5]
	v_cvt_f32_i32_e32 v88, v88
	v_cvt_f32_i32_e32 v89, v89
	v_cvt_f32_i32_e32 v90, v90
	v_cvt_f32_i32_e32 v91, v91
	v_cvt_f32_i32_e32 v80, v80
	v_cvt_f32_i32_e32 v81, v81
	v_cvt_f32_i32_e32 v82, v82
	v_cvt_f32_i32_e32 v83, v83
	v_pk_mul_f32 v[88:89], v[144:145], v[88:89]
	v_pk_mul_f32 v[90:91], v[146:147], v[90:91]
	v_pk_mul_f32 v[80:81], v[148:149], v[80:81]
	v_pk_mul_f32 v[82:83], v[150:151], v[82:83]
	v_pk_fma_f32 v[88:89], v[164:165], v[88:89], v[136:137] op_sel_hi:[0,1,1]
	v_pk_fma_f32 v[90:91], v[164:165], v[90:91], v[138:139] op_sel_hi:[0,1,1]
	v_pk_fma_f32 v[80:81], v[164:165], v[80:81], v[140:141] op_sel_hi:[0,1,1]
	v_pk_fma_f32 v[82:83], v[164:165], v[82:83], v[142:143] op_sel_hi:[0,1,1]
	v_max_f32_e32 v88, s15, v88
	v_max_f32_e32 v89, s15, v89
	v_max_f32_e32 v90, s15, v90
	v_max_f32_e32 v91, s15, v91
	v_max_f32_e32 v80, s15, v80
	v_max_f32_e32 v81, s15, v81
	v_max_f32_e32 v82, s15, v82
	v_max_f32_e32 v83, s15, v83
	v_exp_f32_e32 v156, v88
	v_exp_f32_e32 v157, v89
	v_exp_f32_e32 v158, v90
	v_exp_f32_e32 v159, v91
	v_exp_f32_e32 v160, v80
	v_exp_f32_e32 v161, v81
	v_exp_f32_e32 v184, v82
	v_exp_f32_e32 v185, v83
	v_cvt_f32_i32_e32 v92, v92
	v_cvt_f32_i32_e32 v93, v93
	v_cvt_f32_i32_e32 v94, v94
	v_cvt_f32_i32_e32 v95, v95
	v_cvt_f32_i32_e32 v84, v84
	v_cvt_f32_i32_e32 v85, v85
	v_cvt_f32_i32_e32 v86, v86
	v_cvt_f32_i32_e32 v87, v87
	v_pk_mul_f32 v[92:93], v[152:153], v[92:93]
	v_pk_mul_f32 v[94:95], v[154:155], v[94:95]
	v_pk_mul_f32 v[84:85], v[194:195], v[84:85]
	v_pk_mul_f32 v[86:87], v[196:197], v[86:87]
	v_pk_fma_f32 v[92:93], v[164:165], v[92:93], v[186:187] op_sel_hi:[0,1,1]
	v_pk_fma_f32 v[94:95], v[164:165], v[94:95], v[188:189] op_sel_hi:[0,1,1]
	v_pk_fma_f32 v[84:85], v[164:165], v[84:85], v[190:191] op_sel_hi:[0,1,1]
	v_pk_fma_f32 v[86:87], v[164:165], v[86:87], v[192:193] op_sel_hi:[0,1,1]
	v_pk_add_f32 v[156:157], v[156:157], 1.0 op_sel_hi:[1,0]
	v_pk_add_f32 v[158:159], v[158:159], 1.0 op_sel_hi:[1,0]
	v_pk_add_f32 v[160:161], v[160:161], 1.0 op_sel_hi:[1,0]
	v_pk_add_f32 v[184:185], v[184:185], 1.0 op_sel_hi:[1,0]
	v_rcp_f32_e32 v156, v156
	v_rcp_f32_e32 v157, v157
	v_rcp_f32_e32 v158, v158
	v_rcp_f32_e32 v159, v159
	v_rcp_f32_e32 v160, v160
	v_rcp_f32_e32 v161, v161
	v_rcp_f32_e32 v184, v184
	v_rcp_f32_e32 v185, v185
	v_med3_f32 v92, v92, s14, v135
	v_med3_f32 v93, v93, s14, v135
	v_med3_f32 v94, v94, s14, v135
	v_med3_f32 v95, v95, s14, v135
	v_med3_f32 v84, v84, s14, v135
	v_med3_f32 v85, v85, s14, v135
	v_med3_f32 v86, v86, s14, v135
	v_med3_f32 v87, v87, s14, v135
	v_pk_mul_f32 v[156:157], v[88:89], v[156:157]
	v_pk_mul_f32 v[158:159], v[90:91], v[158:159]
	v_pk_mul_f32 v[160:161], v[80:81], v[160:161]
	v_pk_mul_f32 v[184:185], v[82:83], v[184:185]
	v_pk_mul_f32 v[92:93], v[92:93], v[156:157]
	v_pk_mul_f32 v[94:95], v[94:95], v[158:159]
	v_pk_mul_f32 v[84:85], v[84:85], v[160:161]
	v_pk_mul_f32 v[86:87], v[86:87], v[184:185]
	v_cvt_pk_fp8_f32 v130, v92, v93
	v_cvt_pk_fp8_f32 v131, v84, v85
	v_cvt_pk_fp8_f32 v130, v94, v95 op_sel:[0,0,1]
	v_cvt_pk_fp8_f32 v131, v86, v87 op_sel:[0,0,1]
	v_or_b32_e32 v134, 0x8000, v182
	s_nop 0
	global_store_dwordx2 v134, v[130:131], s[4:5]
	v_cvt_f32_i32_e32 v72, v72
	v_cvt_f32_i32_e32 v73, v73
	v_cvt_f32_i32_e32 v74, v74
	v_cvt_f32_i32_e32 v75, v75
	v_cvt_f32_i32_e32 v64, v64
	v_cvt_f32_i32_e32 v65, v65
	v_cvt_f32_i32_e32 v66, v66
	v_cvt_f32_i32_e32 v67, v67
	v_pk_mul_f32 v[72:73], v[144:145], v[72:73]
	v_pk_mul_f32 v[74:75], v[146:147], v[74:75]
	v_pk_mul_f32 v[64:65], v[148:149], v[64:65]
	v_pk_mul_f32 v[66:67], v[150:151], v[66:67]
	v_pk_fma_f32 v[72:73], v[164:165], v[72:73], v[136:137] op_sel:[1,0,0] op_sel_hi:[1,1,1]
	v_pk_fma_f32 v[74:75], v[164:165], v[74:75], v[138:139] op_sel:[1,0,0] op_sel_hi:[1,1,1]
	v_pk_fma_f32 v[64:65], v[164:165], v[64:65], v[140:141] op_sel:[1,0,0] op_sel_hi:[1,1,1]
	v_pk_fma_f32 v[66:67], v[164:165], v[66:67], v[142:143] op_sel:[1,0,0] op_sel_hi:[1,1,1]
	v_max_f32_e32 v72, s15, v72
	v_max_f32_e32 v73, s15, v73
	v_max_f32_e32 v74, s15, v74
	v_max_f32_e32 v75, s15, v75
	v_max_f32_e32 v64, s15, v64
	v_max_f32_e32 v65, s15, v65
	v_max_f32_e32 v66, s15, v66
	v_max_f32_e32 v67, s15, v67
	v_exp_f32_e32 v156, v72
	v_exp_f32_e32 v157, v73
	v_exp_f32_e32 v158, v74
	v_exp_f32_e32 v159, v75
	v_exp_f32_e32 v160, v64
	v_exp_f32_e32 v161, v65
	v_exp_f32_e32 v184, v66
	v_exp_f32_e32 v185, v67
	v_cvt_f32_i32_e32 v76, v76
	v_cvt_f32_i32_e32 v77, v77
	v_cvt_f32_i32_e32 v78, v78
	v_cvt_f32_i32_e32 v79, v79
	v_cvt_f32_i32_e32 v68, v68
	v_cvt_f32_i32_e32 v69, v69
	v_cvt_f32_i32_e32 v70, v70
	v_cvt_f32_i32_e32 v71, v71
	v_pk_mul_f32 v[76:77], v[152:153], v[76:77]
	v_pk_mul_f32 v[78:79], v[154:155], v[78:79]
	v_pk_mul_f32 v[68:69], v[194:195], v[68:69]
	v_pk_mul_f32 v[70:71], v[196:197], v[70:71]
	v_pk_fma_f32 v[76:77], v[164:165], v[76:77], v[186:187] op_sel:[1,0,0] op_sel_hi:[1,1,1]
	v_pk_fma_f32 v[78:79], v[164:165], v[78:79], v[188:189] op_sel:[1,0,0] op_sel_hi:[1,1,1]
	v_pk_fma_f32 v[68:69], v[164:165], v[68:69], v[190:191] op_sel:[1,0,0] op_sel_hi:[1,1,1]
	v_pk_fma_f32 v[70:71], v[164:165], v[70:71], v[192:193] op_sel:[1,0,0] op_sel_hi:[1,1,1]
	v_pk_add_f32 v[156:157], v[156:157], 1.0 op_sel_hi:[1,0]
	v_pk_add_f32 v[158:159], v[158:159], 1.0 op_sel_hi:[1,0]
	v_pk_add_f32 v[160:161], v[160:161], 1.0 op_sel_hi:[1,0]
	v_pk_add_f32 v[184:185], v[184:185], 1.0 op_sel_hi:[1,0]
	v_rcp_f32_e32 v156, v156
	v_rcp_f32_e32 v157, v157
	v_rcp_f32_e32 v158, v158
	v_rcp_f32_e32 v159, v159
	v_rcp_f32_e32 v160, v160
	v_rcp_f32_e32 v161, v161
	v_rcp_f32_e32 v184, v184
	v_rcp_f32_e32 v185, v185
	v_med3_f32 v76, v76, s14, v135
	v_med3_f32 v77, v77, s14, v135
	v_med3_f32 v78, v78, s14, v135
	v_med3_f32 v79, v79, s14, v135
	v_med3_f32 v68, v68, s14, v135
	v_med3_f32 v69, v69, s14, v135
	v_med3_f32 v70, v70, s14, v135
	v_med3_f32 v71, v71, s14, v135
	v_pk_mul_f32 v[156:157], v[72:73], v[156:157]
	v_pk_mul_f32 v[158:159], v[74:75], v[158:159]
	v_pk_mul_f32 v[160:161], v[64:65], v[160:161]
	v_pk_mul_f32 v[184:185], v[66:67], v[184:185]
	v_pk_mul_f32 v[76:77], v[76:77], v[156:157]
	v_pk_mul_f32 v[78:79], v[78:79], v[158:159]
	v_pk_mul_f32 v[68:69], v[68:69], v[160:161]
	v_pk_mul_f32 v[70:71], v[70:71], v[184:185]
	v_cvt_pk_fp8_f32 v132, v76, v77
	v_cvt_pk_fp8_f32 v133, v68, v69
	v_cvt_pk_fp8_f32 v132, v78, v79 op_sel:[0,0,1]
	v_cvt_pk_fp8_f32 v133, v70, v71 op_sel:[0,0,1]
	v_or_b32_e32 v134, 0xc000, v182
	s_nop 0
	global_store_dwordx2 v134, v[132:133], s[4:5]
	v_cvt_f32_i32_e32 v56, v56
	v_cvt_f32_i32_e32 v57, v57
	v_cvt_f32_i32_e32 v58, v58
	v_cvt_f32_i32_e32 v59, v59
	v_cvt_f32_i32_e32 v48, v48
	v_cvt_f32_i32_e32 v49, v49
	v_cvt_f32_i32_e32 v50, v50
	v_cvt_f32_i32_e32 v51, v51
	v_pk_mul_f32 v[56:57], v[144:145], v[56:57]
	v_pk_mul_f32 v[58:59], v[146:147], v[58:59]
	v_pk_mul_f32 v[48:49], v[148:149], v[48:49]
	v_pk_mul_f32 v[50:51], v[150:151], v[50:51]
	v_pk_fma_f32 v[56:57], v[162:163], v[56:57], v[136:137] op_sel_hi:[0,1,1]
	v_pk_fma_f32 v[58:59], v[162:163], v[58:59], v[138:139] op_sel_hi:[0,1,1]
	v_pk_fma_f32 v[48:49], v[162:163], v[48:49], v[140:141] op_sel_hi:[0,1,1]
	v_pk_fma_f32 v[50:51], v[162:163], v[50:51], v[142:143] op_sel_hi:[0,1,1]
	v_max_f32_e32 v56, s15, v56
	v_max_f32_e32 v57, s15, v57
	v_max_f32_e32 v58, s15, v58
	v_max_f32_e32 v59, s15, v59
	v_max_f32_e32 v48, s15, v48
	v_max_f32_e32 v49, s15, v49
	v_max_f32_e32 v50, s15, v50
	v_max_f32_e32 v51, s15, v51
	v_exp_f32_e32 v156, v56
	v_exp_f32_e32 v157, v57
	v_exp_f32_e32 v158, v58
	v_exp_f32_e32 v159, v59
	v_exp_f32_e32 v160, v48
	v_exp_f32_e32 v161, v49
	v_exp_f32_e32 v184, v50
	v_exp_f32_e32 v185, v51
	v_cvt_f32_i32_e32 v60, v60
	v_cvt_f32_i32_e32 v61, v61
	v_cvt_f32_i32_e32 v62, v62
	v_cvt_f32_i32_e32 v63, v63
	v_cvt_f32_i32_e32 v52, v52
	v_cvt_f32_i32_e32 v53, v53
	v_cvt_f32_i32_e32 v54, v54
	v_cvt_f32_i32_e32 v55, v55
	v_pk_mul_f32 v[60:61], v[152:153], v[60:61]
	v_pk_mul_f32 v[62:63], v[154:155], v[62:63]
	v_pk_mul_f32 v[52:53], v[194:195], v[52:53]
	v_pk_mul_f32 v[54:55], v[196:197], v[54:55]
	v_pk_fma_f32 v[60:61], v[162:163], v[60:61], v[186:187] op_sel_hi:[0,1,1]
	v_pk_fma_f32 v[62:63], v[162:163], v[62:63], v[188:189] op_sel_hi:[0,1,1]
	v_pk_fma_f32 v[52:53], v[162:163], v[52:53], v[190:191] op_sel_hi:[0,1,1]
	v_pk_fma_f32 v[54:55], v[162:163], v[54:55], v[192:193] op_sel_hi:[0,1,1]
	v_pk_add_f32 v[156:157], v[156:157], 1.0 op_sel_hi:[1,0]
	v_pk_add_f32 v[158:159], v[158:159], 1.0 op_sel_hi:[1,0]
	v_pk_add_f32 v[160:161], v[160:161], 1.0 op_sel_hi:[1,0]
	v_pk_add_f32 v[184:185], v[184:185], 1.0 op_sel_hi:[1,0]
	v_rcp_f32_e32 v156, v156
	v_rcp_f32_e32 v157, v157
	v_rcp_f32_e32 v158, v158
	v_rcp_f32_e32 v159, v159
	v_rcp_f32_e32 v160, v160
	v_rcp_f32_e32 v161, v161
	v_rcp_f32_e32 v184, v184
	v_rcp_f32_e32 v185, v185
	v_med3_f32 v60, v60, s14, v135
	v_med3_f32 v61, v61, s14, v135
	v_med3_f32 v62, v62, s14, v135
	v_med3_f32 v63, v63, s14, v135
	v_med3_f32 v52, v52, s14, v135
	v_med3_f32 v53, v53, s14, v135
	v_med3_f32 v54, v54, s14, v135
	v_med3_f32 v55, v55, s14, v135
	v_pk_mul_f32 v[156:157], v[56:57], v[156:157]
	v_pk_mul_f32 v[158:159], v[58:59], v[158:159]
	v_pk_mul_f32 v[160:161], v[48:49], v[160:161]
	v_pk_mul_f32 v[184:185], v[50:51], v[184:185]
	v_pk_mul_f32 v[60:61], v[60:61], v[156:157]
	v_pk_mul_f32 v[62:63], v[62:63], v[158:159]
	v_pk_mul_f32 v[52:53], v[52:53], v[160:161]
	v_pk_mul_f32 v[54:55], v[54:55], v[184:185]
	v_cvt_pk_fp8_f32 v130, v60, v61
	v_cvt_pk_fp8_f32 v131, v52, v53
	v_cvt_pk_fp8_f32 v130, v62, v63 op_sel:[0,0,1]
	v_cvt_pk_fp8_f32 v131, v54, v55 op_sel:[0,0,1]
	v_add_u32_e32 v134, 0x20000, v183
	s_nop 0
	global_store_dwordx2 v134, v[130:131], s[4:5]
	v_cvt_f32_i32_e32 v40, v40
	v_cvt_f32_i32_e32 v41, v41
	v_cvt_f32_i32_e32 v42, v42
	v_cvt_f32_i32_e32 v43, v43
	v_cvt_f32_i32_e32 v32, v32
	v_cvt_f32_i32_e32 v33, v33
	v_cvt_f32_i32_e32 v34, v34
	v_cvt_f32_i32_e32 v35, v35
	v_pk_mul_f32 v[40:41], v[144:145], v[40:41]
	v_pk_mul_f32 v[42:43], v[146:147], v[42:43]
	v_pk_mul_f32 v[32:33], v[148:149], v[32:33]
	v_pk_mul_f32 v[34:35], v[150:151], v[34:35]
	v_pk_fma_f32 v[40:41], v[162:163], v[40:41], v[136:137] op_sel:[1,0,0] op_sel_hi:[1,1,1]
	v_pk_fma_f32 v[42:43], v[162:163], v[42:43], v[138:139] op_sel:[1,0,0] op_sel_hi:[1,1,1]
	v_pk_fma_f32 v[32:33], v[162:163], v[32:33], v[140:141] op_sel:[1,0,0] op_sel_hi:[1,1,1]
	v_pk_fma_f32 v[34:35], v[162:163], v[34:35], v[142:143] op_sel:[1,0,0] op_sel_hi:[1,1,1]
	v_max_f32_e32 v40, s15, v40
	v_max_f32_e32 v41, s15, v41
	v_max_f32_e32 v42, s15, v42
	v_max_f32_e32 v43, s15, v43
	v_max_f32_e32 v32, s15, v32
	v_max_f32_e32 v33, s15, v33
	v_max_f32_e32 v34, s15, v34
	v_max_f32_e32 v35, s15, v35
	v_exp_f32_e32 v156, v40
	v_exp_f32_e32 v157, v41
	v_exp_f32_e32 v158, v42
	v_exp_f32_e32 v159, v43
	v_exp_f32_e32 v160, v32
	v_exp_f32_e32 v161, v33
	v_exp_f32_e32 v184, v34
	v_exp_f32_e32 v185, v35
	v_cvt_f32_i32_e32 v44, v44
	v_cvt_f32_i32_e32 v45, v45
	v_cvt_f32_i32_e32 v46, v46
	v_cvt_f32_i32_e32 v47, v47
	v_cvt_f32_i32_e32 v36, v36
	v_cvt_f32_i32_e32 v37, v37
	v_cvt_f32_i32_e32 v38, v38
	v_cvt_f32_i32_e32 v39, v39
	v_pk_mul_f32 v[44:45], v[152:153], v[44:45]
	v_pk_mul_f32 v[46:47], v[154:155], v[46:47]
	v_pk_mul_f32 v[36:37], v[194:195], v[36:37]
	v_pk_mul_f32 v[38:39], v[196:197], v[38:39]
	v_pk_fma_f32 v[44:45], v[162:163], v[44:45], v[186:187] op_sel:[1,0,0] op_sel_hi:[1,1,1]
	v_pk_fma_f32 v[46:47], v[162:163], v[46:47], v[188:189] op_sel:[1,0,0] op_sel_hi:[1,1,1]
	v_pk_fma_f32 v[36:37], v[162:163], v[36:37], v[190:191] op_sel:[1,0,0] op_sel_hi:[1,1,1]
	v_pk_fma_f32 v[38:39], v[162:163], v[38:39], v[192:193] op_sel:[1,0,0] op_sel_hi:[1,1,1]
	v_pk_add_f32 v[156:157], v[156:157], 1.0 op_sel_hi:[1,0]
	v_pk_add_f32 v[158:159], v[158:159], 1.0 op_sel_hi:[1,0]
	v_pk_add_f32 v[160:161], v[160:161], 1.0 op_sel_hi:[1,0]
	v_pk_add_f32 v[184:185], v[184:185], 1.0 op_sel_hi:[1,0]
	v_rcp_f32_e32 v156, v156
	v_rcp_f32_e32 v157, v157
	v_rcp_f32_e32 v158, v158
	v_rcp_f32_e32 v159, v159
	v_rcp_f32_e32 v160, v160
	v_rcp_f32_e32 v161, v161
	v_rcp_f32_e32 v184, v184
	v_rcp_f32_e32 v185, v185
	v_med3_f32 v44, v44, s14, v135
	v_med3_f32 v45, v45, s14, v135
	v_med3_f32 v46, v46, s14, v135
	v_med3_f32 v47, v47, s14, v135
	v_med3_f32 v36, v36, s14, v135
	v_med3_f32 v37, v37, s14, v135
	v_med3_f32 v38, v38, s14, v135
	v_med3_f32 v39, v39, s14, v135
	v_pk_mul_f32 v[156:157], v[40:41], v[156:157]
	v_pk_mul_f32 v[158:159], v[42:43], v[158:159]
	v_pk_mul_f32 v[160:161], v[32:33], v[160:161]
	v_pk_mul_f32 v[184:185], v[34:35], v[184:185]
	v_pk_mul_f32 v[44:45], v[44:45], v[156:157]
	v_pk_mul_f32 v[46:47], v[46:47], v[158:159]
	v_pk_mul_f32 v[36:37], v[36:37], v[160:161]
	v_pk_mul_f32 v[38:39], v[38:39], v[184:185]
	v_cvt_pk_fp8_f32 v132, v44, v45
	v_cvt_pk_fp8_f32 v133, v36, v37
	v_cvt_pk_fp8_f32 v132, v46, v47 op_sel:[0,0,1]
	v_cvt_pk_fp8_f32 v133, v38, v39 op_sel:[0,0,1]
	v_add_u32_e32 v134, 0x24000, v183
	s_nop 0
	global_store_dwordx2 v134, v[132:133], s[4:5]
	v_cvt_f32_i32_e32 v24, v24
	v_cvt_f32_i32_e32 v25, v25
	v_cvt_f32_i32_e32 v26, v26
	v_cvt_f32_i32_e32 v27, v27
	v_cvt_f32_i32_e32 v16, v16
	v_cvt_f32_i32_e32 v17, v17
	v_cvt_f32_i32_e32 v18, v18
	v_cvt_f32_i32_e32 v19, v19
	v_pk_mul_f32 v[24:25], v[144:145], v[24:25]
	v_pk_mul_f32 v[26:27], v[146:147], v[26:27]
	v_pk_mul_f32 v[16:17], v[148:149], v[16:17]
	v_pk_mul_f32 v[18:19], v[150:151], v[18:19]
	v_pk_fma_f32 v[24:25], v[128:129], v[24:25], v[136:137] op_sel_hi:[0,1,1]
	v_pk_fma_f32 v[26:27], v[128:129], v[26:27], v[138:139] op_sel_hi:[0,1,1]
	v_pk_fma_f32 v[16:17], v[128:129], v[16:17], v[140:141] op_sel_hi:[0,1,1]
	v_pk_fma_f32 v[18:19], v[128:129], v[18:19], v[142:143] op_sel_hi:[0,1,1]
	v_max_f32_e32 v24, s15, v24
	v_max_f32_e32 v25, s15, v25
	v_max_f32_e32 v26, s15, v26
	v_max_f32_e32 v27, s15, v27
	v_max_f32_e32 v16, s15, v16
	v_max_f32_e32 v17, s15, v17
	v_max_f32_e32 v18, s15, v18
	v_max_f32_e32 v19, s15, v19
	v_exp_f32_e32 v156, v24
	v_exp_f32_e32 v157, v25
	v_exp_f32_e32 v158, v26
	v_exp_f32_e32 v159, v27
	v_exp_f32_e32 v160, v16
	v_exp_f32_e32 v161, v17
	v_exp_f32_e32 v184, v18
	v_exp_f32_e32 v185, v19
	v_cvt_f32_i32_e32 v28, v28
	v_cvt_f32_i32_e32 v29, v29
	v_cvt_f32_i32_e32 v30, v30
	v_cvt_f32_i32_e32 v31, v31
	v_cvt_f32_i32_e32 v20, v20
	v_cvt_f32_i32_e32 v21, v21
	v_cvt_f32_i32_e32 v22, v22
	v_cvt_f32_i32_e32 v23, v23
	v_pk_mul_f32 v[28:29], v[152:153], v[28:29]
	v_pk_mul_f32 v[30:31], v[154:155], v[30:31]
	v_pk_mul_f32 v[20:21], v[194:195], v[20:21]
	v_pk_mul_f32 v[22:23], v[196:197], v[22:23]
	v_pk_fma_f32 v[28:29], v[128:129], v[28:29], v[186:187] op_sel_hi:[0,1,1]
	v_pk_fma_f32 v[30:31], v[128:129], v[30:31], v[188:189] op_sel_hi:[0,1,1]
	v_pk_fma_f32 v[20:21], v[128:129], v[20:21], v[190:191] op_sel_hi:[0,1,1]
	v_pk_fma_f32 v[22:23], v[128:129], v[22:23], v[192:193] op_sel_hi:[0,1,1]
	v_pk_add_f32 v[156:157], v[156:157], 1.0 op_sel_hi:[1,0]
	v_pk_add_f32 v[158:159], v[158:159], 1.0 op_sel_hi:[1,0]
	v_pk_add_f32 v[160:161], v[160:161], 1.0 op_sel_hi:[1,0]
	v_pk_add_f32 v[184:185], v[184:185], 1.0 op_sel_hi:[1,0]
	v_rcp_f32_e32 v156, v156
	v_rcp_f32_e32 v157, v157
	v_rcp_f32_e32 v158, v158
	v_rcp_f32_e32 v159, v159
	v_rcp_f32_e32 v160, v160
	v_rcp_f32_e32 v161, v161
	v_rcp_f32_e32 v184, v184
	v_rcp_f32_e32 v185, v185
	v_med3_f32 v28, v28, s14, v135
	v_med3_f32 v29, v29, s14, v135
	v_med3_f32 v30, v30, s14, v135
	v_med3_f32 v31, v31, s14, v135
	v_med3_f32 v20, v20, s14, v135
	v_med3_f32 v21, v21, s14, v135
	v_med3_f32 v22, v22, s14, v135
	v_med3_f32 v23, v23, s14, v135
	v_pk_mul_f32 v[156:157], v[24:25], v[156:157]
	v_pk_mul_f32 v[158:159], v[26:27], v[158:159]
	v_pk_mul_f32 v[160:161], v[16:17], v[160:161]
	v_pk_mul_f32 v[184:185], v[18:19], v[184:185]
	v_pk_mul_f32 v[28:29], v[28:29], v[156:157]
	v_pk_mul_f32 v[30:31], v[30:31], v[158:159]
	v_pk_mul_f32 v[20:21], v[20:21], v[160:161]
	v_pk_mul_f32 v[22:23], v[22:23], v[184:185]
	v_cvt_pk_fp8_f32 v130, v28, v29
	v_cvt_pk_fp8_f32 v131, v20, v21
	v_cvt_pk_fp8_f32 v130, v30, v31 op_sel:[0,0,1]
	v_cvt_pk_fp8_f32 v131, v22, v23 op_sel:[0,0,1]
	v_add_u32_e32 v134, 0x28000, v183
	s_nop 0
	global_store_dwordx2 v134, v[130:131], s[4:5]
	v_cvt_f32_i32_e32 v8, v8
	v_cvt_f32_i32_e32 v9, v9
	v_cvt_f32_i32_e32 v10, v10
	v_cvt_f32_i32_e32 v11, v11
	v_cvt_f32_i32_e32 v0, v0
	v_cvt_f32_i32_e32 v1, v1
	v_cvt_f32_i32_e32 v2, v2
	v_cvt_f32_i32_e32 v3, v3
	v_pk_mul_f32 v[8:9], v[144:145], v[8:9]
	v_pk_mul_f32 v[10:11], v[146:147], v[10:11]
	v_pk_mul_f32 v[0:1], v[148:149], v[0:1]
	v_pk_mul_f32 v[2:3], v[150:151], v[2:3]
	v_pk_fma_f32 v[8:9], v[128:129], v[8:9], v[136:137] op_sel:[1,0,0] op_sel_hi:[1,1,1]
	v_pk_fma_f32 v[10:11], v[128:129], v[10:11], v[138:139] op_sel:[1,0,0] op_sel_hi:[1,1,1]
	v_pk_fma_f32 v[0:1], v[128:129], v[0:1], v[140:141] op_sel:[1,0,0] op_sel_hi:[1,1,1]
	v_pk_fma_f32 v[2:3], v[128:129], v[2:3], v[142:143] op_sel:[1,0,0] op_sel_hi:[1,1,1]
	v_max_f32_e32 v8, s15, v8
	v_max_f32_e32 v9, s15, v9
	v_max_f32_e32 v10, s15, v10
	v_max_f32_e32 v11, s15, v11
	v_max_f32_e32 v0, s15, v0
	v_max_f32_e32 v1, s15, v1
	v_max_f32_e32 v2, s15, v2
	v_max_f32_e32 v3, s15, v3
	v_exp_f32_e32 v156, v8
	v_exp_f32_e32 v157, v9
	v_exp_f32_e32 v158, v10
	v_exp_f32_e32 v159, v11
	v_exp_f32_e32 v160, v0
	v_exp_f32_e32 v161, v1
	v_exp_f32_e32 v184, v2
	v_exp_f32_e32 v185, v3
	v_cvt_f32_i32_e32 v12, v12
	v_cvt_f32_i32_e32 v13, v13
	v_cvt_f32_i32_e32 v14, v14
	v_cvt_f32_i32_e32 v15, v15
	v_cvt_f32_i32_e32 v4, v4
	v_cvt_f32_i32_e32 v5, v5
	v_cvt_f32_i32_e32 v6, v6
	v_cvt_f32_i32_e32 v7, v7
	v_pk_mul_f32 v[12:13], v[152:153], v[12:13]
	v_pk_mul_f32 v[14:15], v[154:155], v[14:15]
	v_pk_mul_f32 v[4:5], v[194:195], v[4:5]
	v_pk_mul_f32 v[6:7], v[196:197], v[6:7]
	v_pk_fma_f32 v[12:13], v[128:129], v[12:13], v[186:187] op_sel:[1,0,0] op_sel_hi:[1,1,1]
	v_pk_fma_f32 v[14:15], v[128:129], v[14:15], v[188:189] op_sel:[1,0,0] op_sel_hi:[1,1,1]
	v_pk_fma_f32 v[4:5], v[128:129], v[4:5], v[190:191] op_sel:[1,0,0] op_sel_hi:[1,1,1]
	v_pk_fma_f32 v[6:7], v[128:129], v[6:7], v[192:193] op_sel:[1,0,0] op_sel_hi:[1,1,1]
	v_pk_add_f32 v[156:157], v[156:157], 1.0 op_sel_hi:[1,0]
	v_pk_add_f32 v[158:159], v[158:159], 1.0 op_sel_hi:[1,0]
	v_pk_add_f32 v[160:161], v[160:161], 1.0 op_sel_hi:[1,0]
	v_pk_add_f32 v[184:185], v[184:185], 1.0 op_sel_hi:[1,0]
	v_rcp_f32_e32 v156, v156
	v_rcp_f32_e32 v157, v157
	v_rcp_f32_e32 v158, v158
	v_rcp_f32_e32 v159, v159
	v_rcp_f32_e32 v160, v160
	v_rcp_f32_e32 v161, v161
	v_rcp_f32_e32 v184, v184
	v_rcp_f32_e32 v185, v185
	v_med3_f32 v12, v12, s14, v135
	v_med3_f32 v13, v13, s14, v135
	v_med3_f32 v14, v14, s14, v135
	v_med3_f32 v15, v15, s14, v135
	v_med3_f32 v4, v4, s14, v135
	v_med3_f32 v5, v5, s14, v135
	v_med3_f32 v6, v6, s14, v135
	v_med3_f32 v7, v7, s14, v135
	v_pk_mul_f32 v[156:157], v[8:9], v[156:157]
	v_pk_mul_f32 v[158:159], v[10:11], v[158:159]
	v_pk_mul_f32 v[160:161], v[0:1], v[160:161]
	v_pk_mul_f32 v[184:185], v[2:3], v[184:185]
	v_pk_mul_f32 v[12:13], v[12:13], v[156:157]
	v_pk_mul_f32 v[14:15], v[14:15], v[158:159]
	v_pk_mul_f32 v[4:5], v[4:5], v[160:161]
	v_pk_mul_f32 v[6:7], v[6:7], v[184:185]
	v_cvt_pk_fp8_f32 v132, v12, v13
	v_cvt_pk_fp8_f32 v133, v4, v5
	v_cvt_pk_fp8_f32 v132, v14, v15 op_sel:[0,0,1]
	v_cvt_pk_fp8_f32 v133, v6, v7 op_sel:[0,0,1]
	v_add_u32_e32 v134, 0x2c000, v183
	s_nop 0
	global_store_dwordx2 v134, v[132:133], s[4:5]
	s_andn2_b64 vcc, exec, s[12:13]
	s_mov_b64 s[4:5], -1
	s_cbranch_vccnz .LBB0_914
	s_andn2_b64 vcc, exec, s[8:9]
	s_cbranch_vccnz .LBB0_913
	s_barrier
	s_branch .LBB0_913
